# v135 plus back-edge rotation: loop-bottom counters and loop-top SALU address block moved into the last MFMA block of 6 GEMM K-loops
# speedup vs baseline: 1.0044x; 1.0044x over previous
.LBB0_187:
	s_add_u32 s48, s36, 0xfff00080
	s_addc_u32 s49, s37, -1
	s_add_i32 s75, 0, 0x10000
	s_cmp_eq_u32 s73, 60
	s_cselect_b32 s53, s23, s49
	s_cselect_b32 s52, s22, s48
	s_cselect_b32 s49, s25, s17
	s_cselect_b32 s48, s24, s15
	s_add_i32 s78, 0, 0x14000
.Lrot_win:
	v_add_u32_e32 v140, s75, v145
	ds_read_b128 v[150:153], v140
	ds_read_b128 v[154:157], v140 offset:1024
	ds_read_b128 v[158:161], v140 offset:2048
	ds_read_b128 v[162:165], v140 offset:3072
	v_add_u32_e32 v140, s78, v145
	ds_read_b128 v[166:169], v140
	ds_read_b128 v[170:173], v140 offset:1024
	ds_read_b128 v[174:177], v140 offset:2048
	ds_read_b128 v[178:181], v140 offset:3072
	v_lshl_add_u64 v[142:143], s[36:37], 0, v[136:137]
	s_add_i32 m0, s64, 0xc000
	ds_read_b128 v[182:185], v149
	ds_read_b128 v[186:189], v149 offset:1024
	ds_read_b128 v[190:193], v149 offset:2048
	ds_read_b128 v[194:197], v149 offset:3072
	ds_read_b128 v[198:201], v149 offset:4096
	ds_read_b128 v[208:211], v149 offset:5120
	ds_read_b128 v[212:215], v149 offset:6144
	ds_read_b128 v[216:219], v149 offset:7168
	global_load_lds_dwordx4 v[142:143], off
	v_lshl_add_u64 v[142:143], s[36:37], 0, v[138:139]
	s_add_i32 m0, s64, 0xe000
	s_nop 0
	global_load_lds_dwordx4 v[142:143], off
	s_waitcnt vmcnt(8)
	s_waitcnt lgkmcnt(0)
	s_barrier
	s_setprio 1
	s_waitcnt lgkmcnt(0)
	v_mfma_f32_16x16x32_bf16 v[126:129], v[150:153], v[182:185], v[126:129]
	v_mfma_f32_16x16x32_bf16 v[122:125], v[158:161], v[182:185], v[122:125]
	v_mfma_f32_16x16x32_bf16 v[110:113], v[150:153], v[190:193], v[110:113]
	v_mfma_f32_16x16x32_bf16 v[106:109], v[158:161], v[190:193], v[106:109]
	v_mfma_f32_16x16x32_bf16 v[92:95], v[150:153], v[198:201], v[92:95]
	v_mfma_f32_16x16x32_bf16 v[88:91], v[158:161], v[198:201], v[88:91]
	v_mfma_f32_16x16x32_bf16 v[76:79], v[150:153], v[212:215], v[76:79]
	v_mfma_f32_16x16x32_bf16 v[72:75], v[158:161], v[212:215], v[72:75]
	v_mfma_f32_16x16x32_bf16 v[126:129], v[154:157], v[186:189], v[126:129]
	v_mfma_f32_16x16x32_bf16 v[122:125], v[162:165], v[186:189], v[122:125]
	v_mfma_f32_16x16x32_bf16 v[110:113], v[154:157], v[194:197], v[110:113]
	v_mfma_f32_16x16x32_bf16 v[106:109], v[162:165], v[194:197], v[106:109]
	v_mfma_f32_16x16x32_bf16 v[92:95], v[154:157], v[208:211], v[92:95]
	v_mfma_f32_16x16x32_bf16 v[88:91], v[162:165], v[208:211], v[88:91]
	v_mfma_f32_16x16x32_bf16 v[76:79], v[154:157], v[216:219], v[76:79]
	v_mfma_f32_16x16x32_bf16 v[72:75], v[162:165], v[216:219], v[72:75]
	s_setprio 0
	s_setprio 1
	v_mfma_f32_16x16x32_bf16 v[118:121], v[166:169], v[182:185], v[118:121]
	v_mfma_f32_16x16x32_bf16 v[114:117], v[174:177], v[182:185], v[114:117]
	v_mfma_f32_16x16x32_bf16 v[102:105], v[166:169], v[190:193], v[102:105]
	v_mfma_f32_16x16x32_bf16 v[98:101], v[174:177], v[190:193], v[98:101]
	v_mfma_f32_16x16x32_bf16 v[84:87], v[166:169], v[198:201], v[84:87]
	v_mfma_f32_16x16x32_bf16 v[80:83], v[174:177], v[198:201], v[80:83]
	v_mfma_f32_16x16x32_bf16 v[68:71], v[166:169], v[212:215], v[68:71]
	v_mfma_f32_16x16x32_bf16 v[64:67], v[174:177], v[212:215], v[64:67]
	v_mfma_f32_16x16x32_bf16 v[118:121], v[170:173], v[186:189], v[118:121]
	v_mfma_f32_16x16x32_bf16 v[114:117], v[178:181], v[186:189], v[114:117]
	v_mfma_f32_16x16x32_bf16 v[102:105], v[170:173], v[194:197], v[102:105]
	v_mfma_f32_16x16x32_bf16 v[98:101], v[178:181], v[194:197], v[98:101]
	v_mfma_f32_16x16x32_bf16 v[84:87], v[170:173], v[208:211], v[84:87]
	v_mfma_f32_16x16x32_bf16 v[80:83], v[178:181], v[208:211], v[80:83]
	v_mfma_f32_16x16x32_bf16 v[68:71], v[170:173], v[216:219], v[68:71]
	v_mfma_f32_16x16x32_bf16 v[64:67], v[178:181], v[216:219], v[64:67]
	s_setprio 0
	s_barrier
	s_add_i32 s75, s75, s63
	v_lshl_add_u64 v[142:143], s[48:49], 0, v[96:97]
	s_mov_b32 m0, s75
	ds_read_b128 v[182:185], v149 offset:16384
	ds_read_b128 v[186:189], v149 offset:17408
	ds_read_b128 v[190:193], v149 offset:18432
	ds_read_b128 v[194:197], v149 offset:19456
	ds_read_b128 v[198:201], v149 offset:20480
	ds_read_b128 v[208:211], v149 offset:21504
	ds_read_b128 v[212:215], v149 offset:22528
	ds_read_b128 v[216:219], v149 offset:23552
	global_load_lds_dwordx4 v[142:143], off
	s_add_i32 m0, s75, 0x2000
	s_add_u32 s76, s48, 0x100000
	v_lshl_add_u64 v[220:221], s[48:49], 0, v[130:131]
	s_addc_u32 s77, s49, 0
	s_add_i32 s75, s78, s63
	global_load_lds_dwordx4 v[220:221], off
	v_lshl_add_u64 v[222:223], s[76:77], 0, v[96:97]
	s_mov_b32 m0, s75
	v_lshl_add_u64 v[224:225], s[52:53], 0, v[132:133]
	global_load_lds_dwordx4 v[222:223], off
	v_lshl_add_u64 v[222:223], s[76:77], 0, v[130:131]
	s_add_i32 m0, s75, 0x2000
	s_nop 0
	global_load_lds_dwordx4 v[222:223], off
	v_lshl_add_u64 v[222:223], s[52:53], 0, v[134:135]
	s_mov_b32 m0, s64
	s_nop 0
	global_load_lds_dwordx4 v[222:223], off
	s_mov_b32 m0, s65
	s_nop 0
	global_load_lds_dwordx4 v[224:225], off
	s_waitcnt vmcnt(8)
	s_waitcnt lgkmcnt(0)
	s_barrier
	s_setprio 1
	s_waitcnt lgkmcnt(0)
	v_mfma_f32_16x16x32_bf16 v[60:63], v[150:153], v[182:185], v[60:63]
	v_mfma_f32_16x16x32_bf16 v[56:59], v[158:161], v[182:185], v[56:59]
	v_mfma_f32_16x16x32_bf16 v[48:51], v[150:153], v[190:193], v[48:51]
	v_mfma_f32_16x16x32_bf16 v[40:43], v[158:161], v[190:193], v[40:43]
	v_mfma_f32_16x16x32_bf16 v[32:35], v[150:153], v[198:201], v[32:35]
	v_mfma_f32_16x16x32_bf16 v[24:27], v[158:161], v[198:201], v[24:27]
	v_mfma_f32_16x16x32_bf16 v[16:19], v[150:153], v[212:215], v[16:19]
	v_mfma_f32_16x16x32_bf16 v[8:11], v[158:161], v[212:215], v[8:11]
	v_mfma_f32_16x16x32_bf16 v[60:63], v[154:157], v[186:189], v[60:63]
	v_mfma_f32_16x16x32_bf16 v[56:59], v[162:165], v[186:189], v[56:59]
	v_mfma_f32_16x16x32_bf16 v[48:51], v[154:157], v[194:197], v[48:51]
	v_mfma_f32_16x16x32_bf16 v[40:43], v[162:165], v[194:197], v[40:43]
	v_mfma_f32_16x16x32_bf16 v[32:35], v[154:157], v[208:211], v[32:35]
	v_mfma_f32_16x16x32_bf16 v[24:27], v[162:165], v[208:211], v[24:27]
	v_mfma_f32_16x16x32_bf16 v[16:19], v[154:157], v[216:219], v[16:19]
	v_mfma_f32_16x16x32_bf16 v[8:11], v[162:165], v[216:219], v[8:11]
	s_setprio 0
	s_setprio 1
	v_mfma_f32_16x16x32_bf16 v[52:55], v[166:169], v[182:185], v[52:55]
	v_mfma_f32_16x16x32_bf16 v[44:47], v[174:177], v[182:185], v[44:47]
	v_mfma_f32_16x16x32_bf16 v[36:39], v[166:169], v[190:193], v[36:39]
	v_mfma_f32_16x16x32_bf16 v[28:31], v[174:177], v[190:193], v[28:31]
	v_mfma_f32_16x16x32_bf16 v[20:23], v[166:169], v[198:201], v[20:23]
	v_mfma_f32_16x16x32_bf16 v[12:15], v[174:177], v[198:201], v[12:15]
	v_mfma_f32_16x16x32_bf16 v[4:7], v[166:169], v[212:215], v[4:7]
	v_mfma_f32_16x16x32_bf16 v[0:3], v[174:177], v[212:215], v[0:3]
	v_mfma_f32_16x16x32_bf16 v[52:55], v[170:173], v[186:189], v[52:55]
	v_mfma_f32_16x16x32_bf16 v[44:47], v[178:181], v[186:189], v[44:47]
	v_mfma_f32_16x16x32_bf16 v[36:39], v[170:173], v[194:197], v[36:39]
	v_mfma_f32_16x16x32_bf16 v[28:31], v[178:181], v[194:197], v[28:31]
	v_mfma_f32_16x16x32_bf16 v[20:23], v[170:173], v[208:211], v[20:23]
	v_mfma_f32_16x16x32_bf16 v[12:15], v[178:181], v[208:211], v[12:15]
	v_mfma_f32_16x16x32_bf16 v[4:7], v[170:173], v[216:219], v[4:7]
	v_mfma_f32_16x16x32_bf16 v[0:3], v[178:181], v[216:219], v[0:3]
	s_setprio 0
	s_barrier
	s_add_i32 s75, 0, 0x18000
	v_add_u32_e32 v140, s75, v145
	s_add_i32 s76, 0, 0x1c000
	ds_read_b128 v[150:153], v140
	ds_read_b128 v[154:157], v140 offset:1024
	ds_read_b128 v[158:161], v140 offset:2048
	ds_read_b128 v[162:165], v140 offset:3072
	v_add_u32_e32 v140, s76, v145
	ds_read_b128 v[166:169], v140
	ds_read_b128 v[170:173], v140 offset:1024
	ds_read_b128 v[174:177], v140 offset:2048
	ds_read_b128 v[178:181], v140 offset:3072
	s_add_u32 s52, s52, 0x100000
	s_addc_u32 s53, s53, 0
	s_mov_b32 m0, s66
	v_lshl_add_u64 v[226:227], s[52:53], 0, v[134:135]
	ds_read_b128 v[182:185], v149 offset:32768
	ds_read_b128 v[186:189], v149 offset:33792
	ds_read_b128 v[190:193], v149 offset:34816
	ds_read_b128 v[194:197], v149 offset:35840
	ds_read_b128 v[198:201], v149 offset:36864
	ds_read_b128 v[208:211], v149 offset:37888
	ds_read_b128 v[212:215], v149 offset:38912
	ds_read_b128 v[216:219], v149 offset:39936
	global_load_lds_dwordx4 v[226:227], off
	v_lshl_add_u64 v[226:227], s[52:53], 0, v[132:133]
	s_mov_b32 m0, s67
	s_nop 0
	global_load_lds_dwordx4 v[226:227], off
	s_waitcnt vmcnt(8)
	s_waitcnt lgkmcnt(0)
	s_barrier
	s_setprio 1
	s_waitcnt lgkmcnt(0)
	v_mfma_f32_16x16x32_bf16 v[126:129], v[150:153], v[182:185], v[126:129]
	v_mfma_f32_16x16x32_bf16 v[122:125], v[158:161], v[182:185], v[122:125]
	v_mfma_f32_16x16x32_bf16 v[110:113], v[150:153], v[190:193], v[110:113]
	v_mfma_f32_16x16x32_bf16 v[106:109], v[158:161], v[190:193], v[106:109]
	v_mfma_f32_16x16x32_bf16 v[92:95], v[150:153], v[198:201], v[92:95]
	v_mfma_f32_16x16x32_bf16 v[88:91], v[158:161], v[198:201], v[88:91]
	v_mfma_f32_16x16x32_bf16 v[76:79], v[150:153], v[212:215], v[76:79]
	v_mfma_f32_16x16x32_bf16 v[72:75], v[158:161], v[212:215], v[72:75]
	v_mfma_f32_16x16x32_bf16 v[126:129], v[154:157], v[186:189], v[126:129]
	v_mfma_f32_16x16x32_bf16 v[122:125], v[162:165], v[186:189], v[122:125]
	v_mfma_f32_16x16x32_bf16 v[110:113], v[154:157], v[194:197], v[110:113]
	v_mfma_f32_16x16x32_bf16 v[106:109], v[162:165], v[194:197], v[106:109]
	v_mfma_f32_16x16x32_bf16 v[92:95], v[154:157], v[208:211], v[92:95]
	v_mfma_f32_16x16x32_bf16 v[88:91], v[162:165], v[208:211], v[88:91]
	v_mfma_f32_16x16x32_bf16 v[76:79], v[154:157], v[216:219], v[76:79]
	v_mfma_f32_16x16x32_bf16 v[72:75], v[162:165], v[216:219], v[72:75]
	s_setprio 0
	s_setprio 1
	v_mfma_f32_16x16x32_bf16 v[118:121], v[166:169], v[182:185], v[118:121]
	v_mfma_f32_16x16x32_bf16 v[114:117], v[174:177], v[182:185], v[114:117]
	v_mfma_f32_16x16x32_bf16 v[102:105], v[166:169], v[190:193], v[102:105]
	v_mfma_f32_16x16x32_bf16 v[98:101], v[174:177], v[190:193], v[98:101]
	v_mfma_f32_16x16x32_bf16 v[84:87], v[166:169], v[198:201], v[84:87]
	v_mfma_f32_16x16x32_bf16 v[80:83], v[174:177], v[198:201], v[80:83]
	v_mfma_f32_16x16x32_bf16 v[68:71], v[166:169], v[212:215], v[68:71]
	v_mfma_f32_16x16x32_bf16 v[64:67], v[174:177], v[212:215], v[64:67]
	v_mfma_f32_16x16x32_bf16 v[118:121], v[170:173], v[186:189], v[118:121]
	v_mfma_f32_16x16x32_bf16 v[114:117], v[178:181], v[186:189], v[114:117]
	v_mfma_f32_16x16x32_bf16 v[102:105], v[170:173], v[194:197], v[102:105]
	v_mfma_f32_16x16x32_bf16 v[98:101], v[178:181], v[194:197], v[98:101]
	v_mfma_f32_16x16x32_bf16 v[84:87], v[170:173], v[208:211], v[84:87]
	v_mfma_f32_16x16x32_bf16 v[80:83], v[178:181], v[208:211], v[80:83]
	v_mfma_f32_16x16x32_bf16 v[68:71], v[170:173], v[216:219], v[68:71]
	v_mfma_f32_16x16x32_bf16 v[64:67], v[178:181], v[216:219], v[64:67]
	s_setprio 0
	s_barrier
	s_add_i32 s52, s75, s63
	v_lshl_add_u64 v[142:143], v[142:143], 0, s[96:97]
	s_mov_b32 m0, s52
	ds_read_b128 v[182:185], v149 offset:49152
	ds_read_b128 v[186:189], v149 offset:50176
	ds_read_b128 v[190:193], v149 offset:51200
	ds_read_b128 v[194:197], v149 offset:52224
	ds_read_b128 v[198:201], v149 offset:53248
	ds_read_b128 v[208:211], v149 offset:54272
	ds_read_b128 v[212:215], v149 offset:55296
	ds_read_b128 v[216:219], v149 offset:56320
	global_load_lds_dwordx4 v[142:143], off
	s_add_i32 m0, s52, 0x2000
	s_add_u32 s48, s48, 0x100080
	v_lshl_add_u64 v[142:143], v[220:221], 0, s[96:97]
	s_addc_u32 s49, s49, 0
	s_add_i32 s52, s76, s63
	global_load_lds_dwordx4 v[142:143], off
	v_lshl_add_u64 v[142:143], s[48:49], 0, v[96:97]
	s_mov_b32 m0, s52
	s_nop 0
	global_load_lds_dwordx4 v[142:143], off
	v_lshl_add_u64 v[142:143], s[48:49], 0, v[130:131]
	s_add_i32 m0, s52, 0x2000
	s_nop 0
	global_load_lds_dwordx4 v[142:143], off
	v_lshl_add_u64 v[142:143], v[222:223], 0, s[96:97]
	s_mov_b32 m0, s68
	s_nop 0
	global_load_lds_dwordx4 v[142:143], off
	v_lshl_add_u64 v[142:143], v[224:225], 0, s[96:97]
	s_mov_b32 m0, s69
	s_nop 0
	global_load_lds_dwordx4 v[142:143], off
	s_waitcnt vmcnt(8)
	s_waitcnt lgkmcnt(0)
	s_barrier
	s_setprio 1
	s_waitcnt lgkmcnt(0)
	v_mfma_f32_16x16x32_bf16 v[60:63], v[150:153], v[182:185], v[60:63]
	v_mfma_f32_16x16x32_bf16 v[56:59], v[158:161], v[182:185], v[56:59]
	v_mfma_f32_16x16x32_bf16 v[48:51], v[150:153], v[190:193], v[48:51]
	s_add_i32 s73, s73, 2
	s_add_u32 s36, s36, 0x100
	v_mfma_f32_16x16x32_bf16 v[40:43], v[158:161], v[190:193], v[40:43]
	s_addc_u32 s37, s37, 0
	s_add_u32 s15, s15, 0x100
	v_mfma_f32_16x16x32_bf16 v[32:35], v[150:153], v[198:201], v[32:35]
	s_addc_u32 s17, s17, 0
	s_add_u32 s48, s36, 0xfff00080
	v_mfma_f32_16x16x32_bf16 v[24:27], v[158:161], v[198:201], v[24:27]
	s_addc_u32 s49, s37, -1
	s_add_i32 s75, 0, 0x10000
	v_mfma_f32_16x16x32_bf16 v[16:19], v[150:153], v[212:215], v[16:19]
	s_cmp_eq_u32 s73, 60
	s_cselect_b32 s53, s23, s49
	v_mfma_f32_16x16x32_bf16 v[8:11], v[158:161], v[212:215], v[8:11]
	s_cselect_b32 s52, s22, s48
	s_cselect_b32 s49, s25, s17
	v_mfma_f32_16x16x32_bf16 v[60:63], v[154:157], v[186:189], v[60:63]
	s_cselect_b32 s48, s24, s15
	s_add_i32 s78, 0, 0x14000
	v_mfma_f32_16x16x32_bf16 v[56:59], v[162:165], v[186:189], v[56:59]
	s_cmp_gt_u32 s73, 61
	v_mfma_f32_16x16x32_bf16 v[48:51], v[154:157], v[194:197], v[48:51]
	v_mfma_f32_16x16x32_bf16 v[40:43], v[162:165], v[194:197], v[40:43]
	v_mfma_f32_16x16x32_bf16 v[32:35], v[154:157], v[208:211], v[32:35]
	v_mfma_f32_16x16x32_bf16 v[24:27], v[162:165], v[208:211], v[24:27]
	v_mfma_f32_16x16x32_bf16 v[16:19], v[154:157], v[216:219], v[16:19]
	v_mfma_f32_16x16x32_bf16 v[8:11], v[162:165], v[216:219], v[8:11]
	s_setprio 0
	s_setprio 1
	v_mfma_f32_16x16x32_bf16 v[52:55], v[166:169], v[182:185], v[52:55]
	v_mfma_f32_16x16x32_bf16 v[44:47], v[174:177], v[182:185], v[44:47]
	v_mfma_f32_16x16x32_bf16 v[36:39], v[166:169], v[190:193], v[36:39]
	v_mfma_f32_16x16x32_bf16 v[28:31], v[174:177], v[190:193], v[28:31]
	v_mfma_f32_16x16x32_bf16 v[20:23], v[166:169], v[198:201], v[20:23]
	v_mfma_f32_16x16x32_bf16 v[12:15], v[174:177], v[198:201], v[12:15]
	v_mfma_f32_16x16x32_bf16 v[4:7], v[166:169], v[212:215], v[4:7]
	v_mfma_f32_16x16x32_bf16 v[0:3], v[174:177], v[212:215], v[0:3]
	v_mfma_f32_16x16x32_bf16 v[52:55], v[170:173], v[186:189], v[52:55]
	v_mfma_f32_16x16x32_bf16 v[44:47], v[178:181], v[186:189], v[44:47]
	v_mfma_f32_16x16x32_bf16 v[36:39], v[170:173], v[194:197], v[36:39]
	v_mfma_f32_16x16x32_bf16 v[28:31], v[178:181], v[194:197], v[28:31]
	v_mfma_f32_16x16x32_bf16 v[20:23], v[170:173], v[208:211], v[20:23]
	v_mfma_f32_16x16x32_bf16 v[12:15], v[178:181], v[208:211], v[12:15]
	v_mfma_f32_16x16x32_bf16 v[4:7], v[170:173], v[216:219], v[4:7]
	v_mfma_f32_16x16x32_bf16 v[0:3], v[178:181], v[216:219], v[0:3]
	s_setprio 0
	s_barrier
	s_cbranch_scc0 .Lrot_win
	s_and_b64 vcc, exec, s[10:11]
	s_cbranch_vccz .LBB0_190
	s_barrier

.Lrot_glu:
	v_add_u32_e32 v76, s68, v209
	v_add_u32_e32 v158, s79, v209
	ds_read_b128 v[56:59], v76
	ds_read_b128 v[60:63], v76 offset:1024
	ds_read_b128 v[72:75], v76 offset:2048
	ds_read_b128 v[76:79], v76 offset:3072
	ds_read_b128 v[130:133], v158
	ds_read_b128 v[142:145], v158 offset:1024
	ds_read_b128 v[154:157], v158 offset:2048
	ds_read_b128 v[158:161], v158 offset:3072
	v_lshl_add_u64 v[200:201], s[52:53], 0, v[184:185]
	s_add_i32 m0, s67, 0xc000
	ds_read_b128 v[162:165], v211
	ds_read_b128 v[166:169], v211 offset:1024
	ds_read_b128 v[170:173], v211 offset:2048
	ds_read_b128 v[174:177], v211 offset:3072
	ds_read_b128 v[188:191], v211 offset:4096
	ds_read_b128 v[192:195], v211 offset:5120
	ds_read_b128 v[196:199], v211 offset:6144
	ds_read_b128 v[212:215], v211 offset:7168
	global_load_lds_dwordx4 v[200:201], off
	v_lshl_add_u64 v[200:201], s[52:53], 0, v[186:187]
	s_add_i32 m0, s67, 0xe000
	s_nop 0
	global_load_lds_dwordx4 v[200:201], off
	s_waitcnt vmcnt(8)
	s_waitcnt lgkmcnt(0)
	s_barrier
	s_setprio 1
	s_waitcnt lgkmcnt(0)
	v_mfma_f32_16x16x32_bf16 v[150:153], v[56:59], v[162:165], v[150:153]
	v_mfma_f32_16x16x32_bf16 v[146:149], v[72:75], v[162:165], v[146:149]
	v_mfma_f32_16x16x32_bf16 v[126:129], v[56:59], v[170:173], v[126:129]
	v_mfma_f32_16x16x32_bf16 v[122:125], v[72:75], v[170:173], v[122:125]
	v_mfma_f32_16x16x32_bf16 v[110:113], v[56:59], v[188:191], v[110:113]
	v_mfma_f32_16x16x32_bf16 v[106:109], v[72:75], v[188:191], v[106:109]
	v_mfma_f32_16x16x32_bf16 v[92:95], v[56:59], v[196:199], v[92:95]
	v_mfma_f32_16x16x32_bf16 v[88:91], v[72:75], v[196:199], v[88:91]
	v_mfma_f32_16x16x32_bf16 v[150:153], v[60:63], v[166:169], v[150:153]
	v_mfma_f32_16x16x32_bf16 v[146:149], v[76:79], v[166:169], v[146:149]
	v_mfma_f32_16x16x32_bf16 v[126:129], v[60:63], v[174:177], v[126:129]
	v_mfma_f32_16x16x32_bf16 v[122:125], v[76:79], v[174:177], v[122:125]
	v_mfma_f32_16x16x32_bf16 v[110:113], v[60:63], v[192:195], v[110:113]
	v_mfma_f32_16x16x32_bf16 v[106:109], v[76:79], v[192:195], v[106:109]
	v_mfma_f32_16x16x32_bf16 v[92:95], v[60:63], v[212:215], v[92:95]
	v_mfma_f32_16x16x32_bf16 v[88:91], v[76:79], v[212:215], v[88:91]
	s_setprio 0
	s_setprio 1
	v_mfma_f32_16x16x32_bf16 v[138:141], v[130:133], v[162:165], v[138:141]
	v_mfma_f32_16x16x32_bf16 v[134:137], v[154:157], v[162:165], v[134:137]
	v_mfma_f32_16x16x32_bf16 v[118:121], v[130:133], v[170:173], v[118:121]
	v_mfma_f32_16x16x32_bf16 v[114:117], v[154:157], v[170:173], v[114:117]
	v_mfma_f32_16x16x32_bf16 v[102:105], v[130:133], v[188:191], v[102:105]
	v_mfma_f32_16x16x32_bf16 v[98:101], v[154:157], v[188:191], v[98:101]
	v_mfma_f32_16x16x32_bf16 v[84:87], v[130:133], v[196:199], v[84:87]
	v_mfma_f32_16x16x32_bf16 v[80:83], v[154:157], v[196:199], v[80:83]
	v_mfma_f32_16x16x32_bf16 v[138:141], v[142:145], v[166:169], v[138:141]
	v_mfma_f32_16x16x32_bf16 v[134:137], v[158:161], v[166:169], v[134:137]
	v_mfma_f32_16x16x32_bf16 v[118:121], v[142:145], v[174:177], v[118:121]
	v_mfma_f32_16x16x32_bf16 v[114:117], v[158:161], v[174:177], v[114:117]
	v_mfma_f32_16x16x32_bf16 v[102:105], v[142:145], v[192:195], v[102:105]
	v_mfma_f32_16x16x32_bf16 v[98:101], v[158:161], v[192:195], v[98:101]
	v_mfma_f32_16x16x32_bf16 v[84:87], v[142:145], v[212:215], v[84:87]
	v_mfma_f32_16x16x32_bf16 v[80:83], v[158:161], v[212:215], v[80:83]
	s_setprio 0
	s_barrier
	s_add_i32 s68, s68, s66
	v_lshl_add_u64 v[200:201], s[56:57], 0, v[96:97]
	s_mov_b32 m0, s68
	ds_read_b128 v[162:165], v211 offset:16384
	ds_read_b128 v[166:169], v211 offset:17408
	ds_read_b128 v[170:173], v211 offset:18432
	ds_read_b128 v[174:177], v211 offset:19456
	ds_read_b128 v[188:191], v211 offset:20480
	ds_read_b128 v[192:195], v211 offset:21504
	ds_read_b128 v[196:199], v211 offset:22528
	ds_read_b128 v[212:215], v211 offset:23552
	global_load_lds_dwordx4 v[200:201], off
	s_add_i32 m0, s68, 0x2000
	s_add_u32 s68, s56, 0x40000
	v_lshl_add_u64 v[216:217], s[56:57], 0, v[182:183]
	s_addc_u32 s69, s57, 0
	s_add_i32 s79, s79, s66
	global_load_lds_dwordx4 v[216:217], off
	v_lshl_add_u64 v[218:219], s[68:69], 0, v[96:97]
	s_mov_b32 m0, s79
	v_lshl_add_u64 v[220:221], s[62:63], 0, v[180:181]
	global_load_lds_dwordx4 v[218:219], off
	v_lshl_add_u64 v[218:219], s[68:69], 0, v[182:183]
	s_add_i32 m0, s79, 0x2000
	s_nop 0
	global_load_lds_dwordx4 v[218:219], off
	v_lshl_add_u64 v[218:219], s[62:63], 0, v[178:179]
	s_mov_b32 m0, s67
	s_nop 0
	global_load_lds_dwordx4 v[218:219], off
	s_mov_b32 m0, s72
	s_nop 0
	global_load_lds_dwordx4 v[220:221], off
	s_waitcnt vmcnt(8)
	s_waitcnt lgkmcnt(0)
	s_barrier
	s_setprio 1
	s_waitcnt lgkmcnt(0)
	v_mfma_f32_16x16x32_bf16 v[68:71], v[56:59], v[162:165], v[68:71]
	v_mfma_f32_16x16x32_bf16 v[64:67], v[72:75], v[162:165], v[64:67]
	v_mfma_f32_16x16x32_bf16 v[44:47], v[56:59], v[170:173], v[44:47]
	v_mfma_f32_16x16x32_bf16 v[40:43], v[72:75], v[170:173], v[40:43]
	v_mfma_f32_16x16x32_bf16 v[28:31], v[56:59], v[188:191], v[28:31]
	v_mfma_f32_16x16x32_bf16 v[24:27], v[72:75], v[188:191], v[24:27]
	v_mfma_f32_16x16x32_bf16 v[12:15], v[56:59], v[196:199], v[12:15]
	v_mfma_f32_16x16x32_bf16 v[8:11], v[72:75], v[196:199], v[8:11]
	v_mfma_f32_16x16x32_bf16 v[68:71], v[60:63], v[166:169], v[68:71]
	v_mfma_f32_16x16x32_bf16 v[64:67], v[76:79], v[166:169], v[64:67]
	v_mfma_f32_16x16x32_bf16 v[44:47], v[60:63], v[174:177], v[44:47]
	v_mfma_f32_16x16x32_bf16 v[40:43], v[76:79], v[174:177], v[40:43]
	v_mfma_f32_16x16x32_bf16 v[28:31], v[60:63], v[192:195], v[28:31]
	v_mfma_f32_16x16x32_bf16 v[24:27], v[76:79], v[192:195], v[24:27]
	v_mfma_f32_16x16x32_bf16 v[12:15], v[60:63], v[212:215], v[12:15]
	v_mfma_f32_16x16x32_bf16 v[8:11], v[76:79], v[212:215], v[8:11]
	s_setprio 0
	s_setprio 1
	v_mfma_f32_16x16x32_bf16 v[52:55], v[130:133], v[162:165], v[52:55]
	v_mfma_f32_16x16x32_bf16 v[48:51], v[154:157], v[162:165], v[48:51]
	v_mfma_f32_16x16x32_bf16 v[36:39], v[130:133], v[170:173], v[36:39]
	v_mfma_f32_16x16x32_bf16 v[32:35], v[154:157], v[170:173], v[32:35]
	v_mfma_f32_16x16x32_bf16 v[20:23], v[130:133], v[188:191], v[20:23]
	v_mfma_f32_16x16x32_bf16 v[16:19], v[154:157], v[188:191], v[16:19]
	v_mfma_f32_16x16x32_bf16 v[4:7], v[130:133], v[196:199], v[4:7]
	v_mfma_f32_16x16x32_bf16 v[0:3], v[154:157], v[196:199], v[0:3]
	v_mfma_f32_16x16x32_bf16 v[52:55], v[142:145], v[166:169], v[52:55]
	v_mfma_f32_16x16x32_bf16 v[48:51], v[158:161], v[166:169], v[48:51]
	v_mfma_f32_16x16x32_bf16 v[36:39], v[142:145], v[174:177], v[36:39]
	v_mfma_f32_16x16x32_bf16 v[32:35], v[158:161], v[174:177], v[32:35]
	v_mfma_f32_16x16x32_bf16 v[20:23], v[142:145], v[192:195], v[20:23]
	v_mfma_f32_16x16x32_bf16 v[16:19], v[158:161], v[192:195], v[16:19]
	v_mfma_f32_16x16x32_bf16 v[4:7], v[142:145], v[212:215], v[4:7]
	v_mfma_f32_16x16x32_bf16 v[0:3], v[158:161], v[212:215], v[0:3]
	s_setprio 0
	s_barrier
	s_add_i32 s68, 0, 0x18000
	s_add_i32 s69, 0, 0x1c000
	v_add_u32_e32 v76, s68, v209
	v_add_u32_e32 v158, s69, v209
	ds_read_b128 v[56:59], v76
	ds_read_b128 v[60:63], v76 offset:1024
	ds_read_b128 v[72:75], v76 offset:2048
	ds_read_b128 v[76:79], v76 offset:3072
	ds_read_b128 v[130:133], v158
	ds_read_b128 v[142:145], v158 offset:1024
	ds_read_b128 v[154:157], v158 offset:2048
	ds_read_b128 v[158:161], v158 offset:3072
	s_add_u32 s62, s62, 0x40000
	s_addc_u32 s63, s63, 0
	s_mov_b32 m0, s73
	v_lshl_add_u64 v[222:223], s[62:63], 0, v[178:179]
	ds_read_b128 v[162:165], v211 offset:32768
	ds_read_b128 v[166:169], v211 offset:33792
	ds_read_b128 v[170:173], v211 offset:34816
	ds_read_b128 v[174:177], v211 offset:35840
	ds_read_b128 v[188:191], v211 offset:36864
	ds_read_b128 v[192:195], v211 offset:37888
	ds_read_b128 v[196:199], v211 offset:38912
	ds_read_b128 v[212:215], v211 offset:39936
	global_load_lds_dwordx4 v[222:223], off
	v_lshl_add_u64 v[222:223], s[62:63], 0, v[180:181]
	s_mov_b32 m0, s75
	s_nop 0
	global_load_lds_dwordx4 v[222:223], off
	s_waitcnt vmcnt(8)
	s_waitcnt lgkmcnt(0)
	s_barrier
	s_setprio 1
	s_waitcnt lgkmcnt(0)
	v_mfma_f32_16x16x32_bf16 v[150:153], v[56:59], v[162:165], v[150:153]
	v_mfma_f32_16x16x32_bf16 v[146:149], v[72:75], v[162:165], v[146:149]
	v_mfma_f32_16x16x32_bf16 v[126:129], v[56:59], v[170:173], v[126:129]
	v_mfma_f32_16x16x32_bf16 v[122:125], v[72:75], v[170:173], v[122:125]
	v_mfma_f32_16x16x32_bf16 v[110:113], v[56:59], v[188:191], v[110:113]
	v_mfma_f32_16x16x32_bf16 v[106:109], v[72:75], v[188:191], v[106:109]
	v_mfma_f32_16x16x32_bf16 v[92:95], v[56:59], v[196:199], v[92:95]
	v_mfma_f32_16x16x32_bf16 v[88:91], v[72:75], v[196:199], v[88:91]
	v_mfma_f32_16x16x32_bf16 v[150:153], v[60:63], v[166:169], v[150:153]
	v_mfma_f32_16x16x32_bf16 v[146:149], v[76:79], v[166:169], v[146:149]
	v_mfma_f32_16x16x32_bf16 v[126:129], v[60:63], v[174:177], v[126:129]
	v_mfma_f32_16x16x32_bf16 v[122:125], v[76:79], v[174:177], v[122:125]
	v_mfma_f32_16x16x32_bf16 v[110:113], v[60:63], v[192:195], v[110:113]
	v_mfma_f32_16x16x32_bf16 v[106:109], v[76:79], v[192:195], v[106:109]
	v_mfma_f32_16x16x32_bf16 v[92:95], v[60:63], v[212:215], v[92:95]
	v_mfma_f32_16x16x32_bf16 v[88:91], v[76:79], v[212:215], v[88:91]
	s_setprio 0
	s_setprio 1
	v_mfma_f32_16x16x32_bf16 v[138:141], v[130:133], v[162:165], v[138:141]
	v_mfma_f32_16x16x32_bf16 v[134:137], v[154:157], v[162:165], v[134:137]
	v_mfma_f32_16x16x32_bf16 v[118:121], v[130:133], v[170:173], v[118:121]
	v_mfma_f32_16x16x32_bf16 v[114:117], v[154:157], v[170:173], v[114:117]
	v_mfma_f32_16x16x32_bf16 v[102:105], v[130:133], v[188:191], v[102:105]
	v_mfma_f32_16x16x32_bf16 v[98:101], v[154:157], v[188:191], v[98:101]
	v_mfma_f32_16x16x32_bf16 v[84:87], v[130:133], v[196:199], v[84:87]
	v_mfma_f32_16x16x32_bf16 v[80:83], v[154:157], v[196:199], v[80:83]
	v_mfma_f32_16x16x32_bf16 v[138:141], v[142:145], v[166:169], v[138:141]
	v_mfma_f32_16x16x32_bf16 v[134:137], v[158:161], v[166:169], v[134:137]
	v_mfma_f32_16x16x32_bf16 v[118:121], v[142:145], v[174:177], v[118:121]
	v_mfma_f32_16x16x32_bf16 v[114:117], v[158:161], v[174:177], v[114:117]
	v_mfma_f32_16x16x32_bf16 v[102:105], v[142:145], v[192:195], v[102:105]
	v_mfma_f32_16x16x32_bf16 v[98:101], v[158:161], v[192:195], v[98:101]
	v_mfma_f32_16x16x32_bf16 v[84:87], v[142:145], v[212:215], v[84:87]
	v_mfma_f32_16x16x32_bf16 v[80:83], v[158:161], v[212:215], v[80:83]
	s_setprio 0
	s_barrier
	s_add_i32 s62, s68, s66
	v_lshl_add_u64 v[200:201], v[200:201], 0, s[96:97]
	s_mov_b32 m0, s62
	ds_read_b128 v[162:165], v211 offset:49152
	ds_read_b128 v[166:169], v211 offset:50176
	ds_read_b128 v[170:173], v211 offset:51200
	ds_read_b128 v[174:177], v211 offset:52224
	ds_read_b128 v[188:191], v211 offset:53248
	ds_read_b128 v[192:195], v211 offset:54272
	ds_read_b128 v[196:199], v211 offset:55296
	ds_read_b128 v[212:215], v211 offset:56320
	global_load_lds_dwordx4 v[200:201], off
	s_add_i32 m0, s62, 0x2000
	s_add_u32 s56, s56, 0x40080
	v_lshl_add_u64 v[200:201], v[216:217], 0, s[96:97]
	s_addc_u32 s57, s57, 0
	s_add_i32 s62, s69, s66
	global_load_lds_dwordx4 v[200:201], off
	v_lshl_add_u64 v[200:201], s[56:57], 0, v[96:97]
	s_mov_b32 m0, s62
	s_nop 0
	global_load_lds_dwordx4 v[200:201], off
	v_lshl_add_u64 v[200:201], s[56:57], 0, v[182:183]
	s_add_i32 m0, s62, 0x2000
	s_nop 0
	global_load_lds_dwordx4 v[200:201], off
	v_lshl_add_u64 v[200:201], v[218:219], 0, s[96:97]
	s_mov_b32 m0, s76
	s_nop 0
	global_load_lds_dwordx4 v[200:201], off
	v_lshl_add_u64 v[200:201], v[220:221], 0, s[96:97]
	s_mov_b32 m0, s77
	s_nop 0
	global_load_lds_dwordx4 v[200:201], off
	s_waitcnt vmcnt(8)
	s_waitcnt lgkmcnt(0)
	s_barrier
	s_setprio 1
	s_waitcnt lgkmcnt(0)
	v_mfma_f32_16x16x32_bf16 v[68:71], v[56:59], v[162:165], v[68:71]
	v_mfma_f32_16x16x32_bf16 v[64:67], v[72:75], v[162:165], v[64:67]
	v_mfma_f32_16x16x32_bf16 v[44:47], v[56:59], v[170:173], v[44:47]
	s_add_i32 s49, s49, 2
	s_add_u32 s52, s52, 0x100
	v_mfma_f32_16x16x32_bf16 v[40:43], v[72:75], v[170:173], v[40:43]
	s_addc_u32 s53, s53, 0
	s_add_u32 s23, s23, 0x100
	v_mfma_f32_16x16x32_bf16 v[28:31], v[56:59], v[188:191], v[28:31]
	s_addc_u32 s25, s25, 0
	s_add_u32 s56, s52, 0xfffc0080
	v_mfma_f32_16x16x32_bf16 v[24:27], v[72:75], v[188:191], v[24:27]
	s_addc_u32 s57, s53, -1
	s_add_i32 s68, 0, 0x10000
	v_mfma_f32_16x16x32_bf16 v[12:15], v[56:59], v[196:199], v[12:15]
	s_cmp_eq_u32 s49, 12
	s_cselect_b32 s63, s29, s57
	v_mfma_f32_16x16x32_bf16 v[8:11], v[72:75], v[196:199], v[8:11]
	s_cselect_b32 s62, s28, s56
	s_cselect_b32 s57, s37, s25
	v_mfma_f32_16x16x32_bf16 v[68:71], v[60:63], v[166:169], v[68:71]
	s_cselect_b32 s56, s36, s23
	s_add_i32 s79, 0, 0x14000
	v_mfma_f32_16x16x32_bf16 v[64:67], v[76:79], v[166:169], v[64:67]
	s_cmp_gt_u32 s49, 13
	v_mfma_f32_16x16x32_bf16 v[44:47], v[60:63], v[174:177], v[44:47]
	v_mfma_f32_16x16x32_bf16 v[40:43], v[76:79], v[174:177], v[40:43]
	v_mfma_f32_16x16x32_bf16 v[28:31], v[60:63], v[192:195], v[28:31]
	v_mfma_f32_16x16x32_bf16 v[24:27], v[76:79], v[192:195], v[24:27]
	v_mfma_f32_16x16x32_bf16 v[12:15], v[60:63], v[212:215], v[12:15]
	v_mfma_f32_16x16x32_bf16 v[8:11], v[76:79], v[212:215], v[8:11]
	s_setprio 0
	s_setprio 1
	v_mfma_f32_16x16x32_bf16 v[52:55], v[130:133], v[162:165], v[52:55]
	v_mfma_f32_16x16x32_bf16 v[48:51], v[154:157], v[162:165], v[48:51]
	v_mfma_f32_16x16x32_bf16 v[36:39], v[130:133], v[170:173], v[36:39]
	v_mfma_f32_16x16x32_bf16 v[32:35], v[154:157], v[170:173], v[32:35]
	v_mfma_f32_16x16x32_bf16 v[20:23], v[130:133], v[188:191], v[20:23]
	v_mfma_f32_16x16x32_bf16 v[16:19], v[154:157], v[188:191], v[16:19]
	v_mfma_f32_16x16x32_bf16 v[4:7], v[130:133], v[196:199], v[4:7]
	v_mfma_f32_16x16x32_bf16 v[0:3], v[154:157], v[196:199], v[0:3]
	v_mfma_f32_16x16x32_bf16 v[52:55], v[142:145], v[166:169], v[52:55]
	v_mfma_f32_16x16x32_bf16 v[48:51], v[158:161], v[166:169], v[48:51]
	v_mfma_f32_16x16x32_bf16 v[36:39], v[142:145], v[174:177], v[36:39]
	v_mfma_f32_16x16x32_bf16 v[32:35], v[158:161], v[174:177], v[32:35]
	v_mfma_f32_16x16x32_bf16 v[20:23], v[142:145], v[192:195], v[20:23]
	v_mfma_f32_16x16x32_bf16 v[16:19], v[158:161], v[192:195], v[16:19]
	v_mfma_f32_16x16x32_bf16 v[4:7], v[142:145], v[212:215], v[4:7]
	v_mfma_f32_16x16x32_bf16 v[0:3], v[158:161], v[212:215], v[0:3]
	s_setprio 0
	s_barrier
	s_cbranch_scc0 .Lrot_glu
	s_and_b64 vcc, exec, s[16:17]
	s_cbranch_vccz .LBB0_520
	s_barrier

.Lrot_mgu:
	v_add_u32_e32 v0, s15, v209
	v_add_u32_e32 v1, s15, v210
	v_add_u32_e32 v4, s16, v209
	v_add_u32_e32 v12, s16, v210
	ds_read_b128 v[24:27], v0
	ds_read_b128 v[16:19], v0 offset:2048
	ds_read_b128 v[28:31], v1
	ds_read_b128 v[20:23], v1 offset:2048
	ds_read_b128 v[0:3], v4
	ds_read_b128 v[8:11], v4 offset:2048
	ds_read_b128 v[4:7], v12
	ds_read_b128 v[12:15], v12 offset:2048
	v_cndmask_b32_e32 v96, v166, v219, vcc
	v_cndmask_b32_e32 v169, v168, v220, vcc
	v_cndmask_b32_e32 v190, v178, v221, vcc
	v_lshl_add_u64 v[186:187], v[184:185], 0, s[6:7]
	s_add_i32 m0, s77, 0xc000
	ds_read_b128 v[224:227], v217
	ds_read_b128 v[232:235], v217 offset:2048
	ds_read_b128 v[228:231], v218
	ds_read_b128 v[236:239], v218 offset:2048
	ds_read_b128 v[240:243], v217 offset:4096
	ds_read_b128 v[170:173], v217 offset:6144
	ds_read_b128 v[244:247], v218 offset:4096
	ds_read_b128 v[174:177], v218 offset:6144
	global_load_lds_dwordx4 v[186:187], off
	v_lshl_add_u64 v[186:187], v[182:183], 0, s[6:7]
	s_add_i32 m0, s77, 0xe000
	s_nop 0
	global_load_lds_dwordx4 v[186:187], off
	s_waitcnt vmcnt(8)
	s_waitcnt lgkmcnt(0)
	s_barrier
	s_setprio 1
	s_waitcnt lgkmcnt(0)
	v_mfma_scale_f32_16x16x128_f8f6f4 v[158:161], v[24:31], v[224:231], v[158:161], v199, v198 op_sel_hi:[0,0,0]
	v_mfma_scale_f32_16x16x128_f8f6f4 v[150:153], v[16:23], v[224:231], v[150:153], v199, v198 op_sel_hi:[0,0,0]
	v_mfma_scale_f32_16x16x128_f8f6f4 v[142:145], v[24:31], v[232:239], v[142:145], v199, v198 op_sel_hi:[0,0,0]
	v_mfma_scale_f32_16x16x128_f8f6f4 v[134:137], v[16:23], v[232:239], v[134:137], v199, v198 op_sel_hi:[0,0,0]
	v_mfma_scale_f32_16x16x128_f8f6f4 v[126:129], v[24:31], v[240:247], v[126:129], v199, v198 op_sel_hi:[0,0,0]
	v_mfma_scale_f32_16x16x128_f8f6f4 v[118:121], v[16:23], v[240:247], v[118:121], v199, v198 op_sel_hi:[0,0,0]
	v_mfma_scale_f32_16x16x128_f8f6f4 v[110:113], v[24:31], v[170:177], v[110:113], v199, v198 op_sel_hi:[0,0,0]
	v_mfma_scale_f32_16x16x128_f8f6f4 v[102:105], v[16:23], v[170:177], v[102:105], v199, v198 op_sel_hi:[0,0,0]
	s_setprio 0
	s_setprio 1
	v_mfma_scale_f32_16x16x128_f8f6f4 v[154:157], v[0:7], v[224:231], v[154:157], v199, v198 op_sel_hi:[0,0,0]
	v_mfma_scale_f32_16x16x128_f8f6f4 v[146:149], v[8:15], v[224:231], v[146:149], v199, v198 op_sel_hi:[0,0,0]
	v_mfma_scale_f32_16x16x128_f8f6f4 v[138:141], v[0:7], v[232:239], v[138:141], v199, v198 op_sel_hi:[0,0,0]
	v_mfma_scale_f32_16x16x128_f8f6f4 v[130:133], v[8:15], v[232:239], v[130:133], v199, v198 op_sel_hi:[0,0,0]
	v_mfma_scale_f32_16x16x128_f8f6f4 v[122:125], v[0:7], v[240:247], v[122:125], v199, v198 op_sel_hi:[0,0,0]
	v_mfma_scale_f32_16x16x128_f8f6f4 v[114:117], v[8:15], v[240:247], v[114:117], v199, v198 op_sel_hi:[0,0,0]
	v_mfma_scale_f32_16x16x128_f8f6f4 v[106:109], v[0:7], v[170:177], v[106:109], v199, v198 op_sel_hi:[0,0,0]
	v_mfma_scale_f32_16x16x128_f8f6f4 v[98:101], v[8:15], v[170:177], v[98:101], v199, v198 op_sel_hi:[0,0,0]
	s_setprio 0
	s_barrier
	s_add_i32 s15, s15, s59
	v_lshl_add_u64 v[186:187], s[8:9], 0, v[164:165]
	s_mov_b32 m0, s15
	ds_read_b128 v[170:173], v217 offset:16384
	ds_read_b128 v[224:227], v217 offset:18432
	ds_read_b128 v[174:177], v218 offset:16384
	ds_read_b128 v[228:231], v218 offset:18432
	ds_read_b128 v[232:235], v217 offset:20480
	ds_read_b128 v[240:243], v217 offset:22528
	ds_read_b128 v[236:239], v218 offset:20480
	ds_read_b128 v[244:247], v218 offset:22528
	global_load_lds_dwordx4 v[186:187], off
	s_add_i32 m0, s15, 0x2000
	s_add_u32 s18, s8, 0x80000
	v_lshl_add_u64 v[188:189], s[8:9], 0, v[162:163]
	s_addc_u32 s19, s9, 0
	s_add_i32 s15, s16, s59
	global_load_lds_dwordx4 v[188:189], off
	v_lshl_add_u64 v[192:193], s[18:19], 0, v[164:165]
	s_mov_b32 m0, s15
	v_mov_b32_e32 v191, v97
	global_load_lds_dwordx4 v[192:193], off
	v_lshl_add_u64 v[192:193], s[18:19], 0, v[162:163]
	s_add_i32 m0, s15, 0x2000
	s_nop 0
	global_load_lds_dwordx4 v[192:193], off
	s_mov_b32 m0, s77
	v_lshl_add_u64 v[192:193], s[10:11], 0, v[96:97]
	global_load_lds_dwordx4 v96, s[10:11]
	s_mov_b32 m0, s68
	s_nop 0
	global_load_lds_dwordx4 v190, s[10:11]
	s_waitcnt vmcnt(8)
	s_waitcnt lgkmcnt(0)
	v_lshl_add_u64 v[190:191], s[10:11], 0, v[190:191]
	s_barrier
	s_setprio 1
	s_waitcnt lgkmcnt(0)
	v_mfma_scale_f32_16x16x128_f8f6f4 v[92:95], v[24:31], v[170:177], v[92:95], v199, v198 op_sel_hi:[0,0,0]
	v_mfma_scale_f32_16x16x128_f8f6f4 v[84:87], v[16:23], v[170:177], v[84:87], v199, v198 op_sel_hi:[0,0,0]
	v_mfma_scale_f32_16x16x128_f8f6f4 v[76:79], v[24:31], v[224:231], v[76:79], v199, v198 op_sel_hi:[0,0,0]
	v_mfma_scale_f32_16x16x128_f8f6f4 v[68:71], v[16:23], v[224:231], v[68:71], v199, v198 op_sel_hi:[0,0,0]
	v_mfma_scale_f32_16x16x128_f8f6f4 v[60:63], v[24:31], v[232:239], v[60:63], v199, v198 op_sel_hi:[0,0,0]
	v_mfma_scale_f32_16x16x128_f8f6f4 v[52:55], v[16:23], v[232:239], v[52:55], v199, v198 op_sel_hi:[0,0,0]
	v_mfma_scale_f32_16x16x128_f8f6f4 v[44:47], v[24:31], v[240:247], v[44:47], v199, v198 op_sel_hi:[0,0,0]
	v_mfma_scale_f32_16x16x128_f8f6f4 v[36:39], v[16:23], v[240:247], v[36:39], v199, v198 op_sel_hi:[0,0,0]
	s_setprio 0
	s_setprio 1
	v_mfma_scale_f32_16x16x128_f8f6f4 v[88:91], v[0:7], v[170:177], v[88:91], v199, v198 op_sel_hi:[0,0,0]
	v_mfma_scale_f32_16x16x128_f8f6f4 v[80:83], v[8:15], v[170:177], v[80:83], v199, v198 op_sel_hi:[0,0,0]
	v_mfma_scale_f32_16x16x128_f8f6f4 v[72:75], v[0:7], v[224:231], v[72:75], v199, v198 op_sel_hi:[0,0,0]
	v_mfma_scale_f32_16x16x128_f8f6f4 v[64:67], v[8:15], v[224:231], v[64:67], v199, v198 op_sel_hi:[0,0,0]
	v_mfma_scale_f32_16x16x128_f8f6f4 v[56:59], v[0:7], v[232:239], v[56:59], v199, v198 op_sel_hi:[0,0,0]
	v_mfma_scale_f32_16x16x128_f8f6f4 v[48:51], v[8:15], v[232:239], v[48:51], v199, v198 op_sel_hi:[0,0,0]
	v_mfma_scale_f32_16x16x128_f8f6f4 v[40:43], v[0:7], v[240:247], v[40:43], v199, v198 op_sel_hi:[0,0,0]
	v_mfma_scale_f32_16x16x128_f8f6f4 v[32:35], v[8:15], v[240:247], v[32:35], v199, v198 op_sel_hi:[0,0,0]
	s_setprio 0
	s_barrier
	s_add_i32 s15, 0, 0x18000
	s_add_i32 s16, 0, 0x1c000
	v_add_u32_e32 v0, s15, v209
	v_add_u32_e32 v1, s15, v210
	v_add_u32_e32 v4, s16, v209
	v_add_u32_e32 v12, s16, v210
	ds_read_b128 v[16:19], v0
	ds_read_b128 v[24:27], v0 offset:2048
	ds_read_b128 v[20:23], v1
	ds_read_b128 v[28:31], v1 offset:2048
	ds_read_b128 v[0:3], v4
	ds_read_b128 v[8:11], v4 offset:2048
	ds_read_b128 v[4:7], v12
	ds_read_b128 v[12:15], v12 offset:2048
	s_mov_b32 m0, s69
	ds_read_b128 v[170:173], v217 offset:32768
	ds_read_b128 v[224:227], v217 offset:34816
	ds_read_b128 v[174:177], v218 offset:32768
	ds_read_b128 v[228:231], v218 offset:34816
	ds_read_b128 v[232:235], v217 offset:36864
	ds_read_b128 v[240:243], v217 offset:38912
	ds_read_b128 v[236:239], v218 offset:36864
	ds_read_b128 v[244:247], v218 offset:38912
	v_cndmask_b32_e32 v96, v180, v222, vcc
	global_load_lds_dwordx4 v169, s[10:11]
	s_mov_b32 m0, s48
	s_nop 0
	global_load_lds_dwordx4 v96, s[10:11]
	s_waitcnt vmcnt(8)
	s_waitcnt lgkmcnt(0)
	s_barrier
	s_setprio 1
	s_waitcnt lgkmcnt(0)
	v_mfma_scale_f32_16x16x128_f8f6f4 v[158:161], v[16:23], v[170:177], v[158:161], v199, v198 op_sel_hi:[0,0,0]
	v_mfma_scale_f32_16x16x128_f8f6f4 v[150:153], v[24:31], v[170:177], v[150:153], v199, v198 op_sel_hi:[0,0,0]
	v_mfma_scale_f32_16x16x128_f8f6f4 v[142:145], v[16:23], v[224:231], v[142:145], v199, v198 op_sel_hi:[0,0,0]
	v_mfma_scale_f32_16x16x128_f8f6f4 v[134:137], v[24:31], v[224:231], v[134:137], v199, v198 op_sel_hi:[0,0,0]
	v_mfma_scale_f32_16x16x128_f8f6f4 v[126:129], v[16:23], v[232:239], v[126:129], v199, v198 op_sel_hi:[0,0,0]
	v_mfma_scale_f32_16x16x128_f8f6f4 v[118:121], v[24:31], v[232:239], v[118:121], v199, v198 op_sel_hi:[0,0,0]
	v_mfma_scale_f32_16x16x128_f8f6f4 v[110:113], v[16:23], v[240:247], v[110:113], v199, v198 op_sel_hi:[0,0,0]
	v_mfma_scale_f32_16x16x128_f8f6f4 v[102:105], v[24:31], v[240:247], v[102:105], v199, v198 op_sel_hi:[0,0,0]
	s_setprio 0
	s_setprio 1
	v_mfma_scale_f32_16x16x128_f8f6f4 v[154:157], v[0:7], v[170:177], v[154:157], v199, v198 op_sel_hi:[0,0,0]
	v_mfma_scale_f32_16x16x128_f8f6f4 v[146:149], v[8:15], v[170:177], v[146:149], v199, v198 op_sel_hi:[0,0,0]
	v_mfma_scale_f32_16x16x128_f8f6f4 v[138:141], v[0:7], v[224:231], v[138:141], v199, v198 op_sel_hi:[0,0,0]
	v_mfma_scale_f32_16x16x128_f8f6f4 v[130:133], v[8:15], v[224:231], v[130:133], v199, v198 op_sel_hi:[0,0,0]
	v_mfma_scale_f32_16x16x128_f8f6f4 v[122:125], v[0:7], v[232:239], v[122:125], v199, v198 op_sel_hi:[0,0,0]
	v_mfma_scale_f32_16x16x128_f8f6f4 v[114:117], v[8:15], v[232:239], v[114:117], v199, v198 op_sel_hi:[0,0,0]
	v_mfma_scale_f32_16x16x128_f8f6f4 v[106:109], v[0:7], v[240:247], v[106:109], v199, v198 op_sel_hi:[0,0,0]
	v_mfma_scale_f32_16x16x128_f8f6f4 v[98:101], v[8:15], v[240:247], v[98:101], v199, v198 op_sel_hi:[0,0,0]
	s_setprio 0
	s_barrier
	s_add_i32 s10, s15, s59
	v_lshl_add_u64 v[186:187], v[186:187], 0, s[96:97]
	s_mov_b32 m0, s10
	ds_read_b128 v[170:173], v217 offset:49152
	ds_read_b128 v[224:227], v217 offset:51200
	ds_read_b128 v[174:177], v218 offset:49152
	ds_read_b128 v[228:231], v218 offset:51200
	ds_read_b128 v[232:235], v217 offset:53248
	ds_read_b128 v[240:243], v217 offset:55296
	ds_read_b128 v[236:239], v218 offset:53248
	ds_read_b128 v[244:247], v218 offset:55296
	global_load_lds_dwordx4 v[186:187], off
	s_add_i32 m0, s10, 0x2000
	s_add_u32 s8, s8, 0x80080
	v_lshl_add_u64 v[186:187], v[188:189], 0, s[96:97]
	s_addc_u32 s9, s9, 0
	s_add_i32 s10, s16, s59
	global_load_lds_dwordx4 v[186:187], off
	v_lshl_add_u64 v[186:187], s[8:9], 0, v[164:165]
	s_mov_b32 m0, s10
	s_nop 0
	global_load_lds_dwordx4 v[186:187], off
	v_lshl_add_u64 v[186:187], s[8:9], 0, v[162:163]
	s_add_i32 m0, s10, 0x2000
	s_nop 0
	global_load_lds_dwordx4 v[186:187], off
	v_lshl_add_u64 v[186:187], v[192:193], 0, s[96:97]
	s_mov_b32 m0, s49
	s_nop 0
	global_load_lds_dwordx4 v[186:187], off
	v_lshl_add_u64 v[186:187], v[190:191], 0, s[96:97]
	s_mov_b32 m0, s87
	s_nop 0
	global_load_lds_dwordx4 v[186:187], off
	s_waitcnt vmcnt(8)
	s_waitcnt lgkmcnt(0)
	s_barrier
	s_setprio 1
	s_waitcnt lgkmcnt(0)
	v_mfma_scale_f32_16x16x128_f8f6f4 v[92:95], v[16:23], v[170:177], v[92:95], v199, v198 op_sel_hi:[0,0,0]
	v_mfma_scale_f32_16x16x128_f8f6f4 v[84:87], v[24:31], v[170:177], v[84:87], v199, v198 op_sel_hi:[0,0,0]
	v_mfma_scale_f32_16x16x128_f8f6f4 v[76:79], v[16:23], v[224:231], v[76:79], v199, v198 op_sel_hi:[0,0,0]
	s_add_i32 s14, s14, 2
	s_add_u32 s6, s6, 0x100
	v_mfma_scale_f32_16x16x128_f8f6f4 v[68:71], v[24:31], v[224:231], v[68:71], v199, v198 op_sel_hi:[0,0,0]
	s_addc_u32 s7, s7, 0
	s_add_u32 s8, s90, s6
	v_mfma_scale_f32_16x16x128_f8f6f4 v[60:63], v[16:23], v[232:239], v[60:63], v199, v198 op_sel_hi:[0,0,0]
	s_addc_u32 s9, s91, s7
	s_add_u32 s10, s8, 0x3f800100
	v_mfma_scale_f32_16x16x128_f8f6f4 v[52:55], v[24:31], v[232:239], v[52:55], v199, v198 op_sel_hi:[0,0,0]
	s_addc_u32 s11, s9, 0
	s_add_u32 s16, s12, s6
	v_mfma_scale_f32_16x16x128_f8f6f4 v[44:47], v[16:23], v[240:247], v[44:47], v199, v198 op_sel_hi:[0,0,0]
	s_addc_u32 s17, s13, s7
	s_add_i32 s15, 0, 0x10000
	v_mfma_scale_f32_16x16x128_f8f6f4 v[36:39], v[24:31], v[240:247], v[36:39], v199, v198 op_sel_hi:[0,0,0]
	s_cmpk_eq_i32 s6, 0xf00
	s_cselect_b64 vcc, -1, 0
	s_setprio 0
	s_setprio 1
	v_mfma_scale_f32_16x16x128_f8f6f4 v[88:91], v[0:7], v[170:177], v[88:91], v199, v198 op_sel_hi:[0,0,0]
	s_and_b64 s[8:9], vcc, exec
	s_cselect_b32 s11, s21, s11
	v_mfma_scale_f32_16x16x128_f8f6f4 v[80:83], v[8:15], v[170:177], v[80:83], v199, v198 op_sel_hi:[0,0,0]
	s_cselect_b32 s10, s20, s10
	s_cselect_b32 s9, s73, s17
	v_mfma_scale_f32_16x16x128_f8f6f4 v[72:75], v[0:7], v[224:231], v[72:75], v199, v198 op_sel_hi:[0,0,0]
	s_cselect_b32 s8, s72, s16
	s_add_i32 s16, 0, 0x14000
	v_mfma_scale_f32_16x16x128_f8f6f4 v[64:67], v[8:15], v[224:231], v[64:67], v199, v198 op_sel_hi:[0,0,0]
	s_cmp_gt_u32 s14, 29
	v_mfma_scale_f32_16x16x128_f8f6f4 v[56:59], v[0:7], v[232:239], v[56:59], v199, v198 op_sel_hi:[0,0,0]
	v_mfma_scale_f32_16x16x128_f8f6f4 v[48:51], v[8:15], v[232:239], v[48:51], v199, v198 op_sel_hi:[0,0,0]
	v_mfma_scale_f32_16x16x128_f8f6f4 v[40:43], v[0:7], v[240:247], v[40:43], v199, v198 op_sel_hi:[0,0,0]
	v_mfma_scale_f32_16x16x128_f8f6f4 v[32:35], v[8:15], v[240:247], v[32:35], v199, v198 op_sel_hi:[0,0,0]
	s_setprio 0
	s_barrier
	s_cbranch_scc0 .Lrot_mgu
	s_and_b64 vcc, exec, s[36:37]
	s_cbranch_vccz .LBB0_768
	s_barrier

.Lrot_dgu:
	v_add_u32_e32 v0, s63, v191
	v_add_u32_e32 v1, s63, v192
	v_add_u32_e32 v4, s64, v191
	v_add_u32_e32 v12, s64, v192
	ds_read_b128 v[16:19], v0
	ds_read_b128 v[24:27], v0 offset:2048
	ds_read_b128 v[20:23], v1
	ds_read_b128 v[28:31], v1 offset:2048
	ds_read_b128 v[0:3], v4
	ds_read_b128 v[8:11], v4 offset:2048
	ds_read_b128 v[4:7], v12
	ds_read_b128 v[12:15], v12 offset:2048
	v_lshl_add_u64 v[170:171], s[14:15], 0, v[168:169]
	s_add_i32 m0, s52, 0xc000
	ds_read_b128 v[180:183], v194
	ds_read_b128 v[208:211], v194 offset:2048
	ds_read_b128 v[184:187], v195
	ds_read_b128 v[212:215], v195 offset:2048
	ds_read_b128 v[216:219], v194 offset:4096
	ds_read_b128 v[224:227], v194 offset:6144
	ds_read_b128 v[220:223], v195 offset:4096
	ds_read_b128 v[228:231], v195 offset:6144
	global_load_lds_dwordx4 v[170:171], off
	v_lshl_add_u64 v[170:171], s[14:15], 0, v[178:179]
	s_add_i32 m0, s52, 0xe000
	s_nop 0
	global_load_lds_dwordx4 v[170:171], off
	s_waitcnt vmcnt(8)
	s_waitcnt lgkmcnt(0)
	s_barrier
	s_setprio 1
	s_waitcnt lgkmcnt(0)
	v_mfma_scale_f32_16x16x128_f8f6f4 v[158:161], v[16:23], v[180:187], v[158:161], v189, v188 op_sel_hi:[0,0,0]
	v_mfma_scale_f32_16x16x128_f8f6f4 v[150:153], v[24:31], v[180:187], v[150:153], v189, v188 op_sel_hi:[0,0,0]
	v_mfma_scale_f32_16x16x128_f8f6f4 v[142:145], v[16:23], v[208:215], v[142:145], v189, v188 op_sel_hi:[0,0,0]
	v_mfma_scale_f32_16x16x128_f8f6f4 v[134:137], v[24:31], v[208:215], v[134:137], v189, v188 op_sel_hi:[0,0,0]
	v_mfma_scale_f32_16x16x128_f8f6f4 v[126:129], v[16:23], v[216:223], v[126:129], v189, v188 op_sel_hi:[0,0,0]
	v_mfma_scale_f32_16x16x128_f8f6f4 v[118:121], v[24:31], v[216:223], v[118:121], v189, v188 op_sel_hi:[0,0,0]
	v_mfma_scale_f32_16x16x128_f8f6f4 v[110:113], v[16:23], v[224:231], v[110:113], v189, v188 op_sel_hi:[0,0,0]
	v_mfma_scale_f32_16x16x128_f8f6f4 v[102:105], v[24:31], v[224:231], v[102:105], v189, v188 op_sel_hi:[0,0,0]
	s_setprio 0
	s_setprio 1
	v_mfma_scale_f32_16x16x128_f8f6f4 v[154:157], v[0:7], v[180:187], v[154:157], v189, v188 op_sel_hi:[0,0,0]
	v_mfma_scale_f32_16x16x128_f8f6f4 v[146:149], v[8:15], v[180:187], v[146:149], v189, v188 op_sel_hi:[0,0,0]
	v_mfma_scale_f32_16x16x128_f8f6f4 v[138:141], v[0:7], v[208:215], v[138:141], v189, v188 op_sel_hi:[0,0,0]
	v_mfma_scale_f32_16x16x128_f8f6f4 v[130:133], v[8:15], v[208:215], v[130:133], v189, v188 op_sel_hi:[0,0,0]
	v_mfma_scale_f32_16x16x128_f8f6f4 v[122:125], v[0:7], v[216:223], v[122:125], v189, v188 op_sel_hi:[0,0,0]
	v_mfma_scale_f32_16x16x128_f8f6f4 v[114:117], v[8:15], v[216:223], v[114:117], v189, v188 op_sel_hi:[0,0,0]
	v_mfma_scale_f32_16x16x128_f8f6f4 v[106:109], v[0:7], v[224:231], v[106:109], v189, v188 op_sel_hi:[0,0,0]
	v_mfma_scale_f32_16x16x128_f8f6f4 v[98:101], v[8:15], v[224:231], v[98:101], v189, v188 op_sel_hi:[0,0,0]
	s_setprio 0
	s_barrier
	s_add_i32 s63, s63, s59
	v_lshl_add_u64 v[180:181], s[16:17], 0, v[96:97]
	s_mov_b32 m0, s63
	ds_read_b128 v[208:211], v194 offset:16384
	ds_read_b128 v[216:219], v194 offset:18432
	ds_read_b128 v[212:215], v195 offset:16384
	ds_read_b128 v[220:223], v195 offset:18432
	ds_read_b128 v[224:227], v194 offset:20480
	ds_read_b128 v[232:235], v194 offset:22528
	ds_read_b128 v[228:231], v195 offset:20480
	ds_read_b128 v[236:239], v195 offset:22528
	global_load_lds_dwordx4 v[180:181], off
	s_add_i32 m0, s63, 0x2000
	s_add_u32 s66, s16, 0x80000
	v_lshl_add_u64 v[182:183], s[16:17], 0, v[162:163]
	s_addc_u32 s67, s17, 0
	s_add_i32 s63, s64, s59
	global_load_lds_dwordx4 v[182:183], off
	v_lshl_add_u64 v[170:171], s[66:67], 0, v[96:97]
	s_mov_b32 m0, s63
	v_lshl_add_u64 v[184:185], s[18:19], 0, v[166:167]
	global_load_lds_dwordx4 v[170:171], off
	v_lshl_add_u64 v[170:171], s[66:67], 0, v[162:163]
	s_add_i32 m0, s63, 0x2000
	v_lshl_add_u64 v[186:187], s[18:19], 0, v[164:165]
	global_load_lds_dwordx4 v[170:171], off
	s_mov_b32 m0, s52
	s_nop 0
	global_load_lds_dwordx4 v[184:185], off
	s_mov_b32 m0, s53
	s_nop 0
	global_load_lds_dwordx4 v[186:187], off
	s_waitcnt vmcnt(8)
	s_waitcnt lgkmcnt(0)
	s_barrier
	s_setprio 1
	s_waitcnt lgkmcnt(0)
	v_mfma_scale_f32_16x16x128_f8f6f4 v[92:95], v[16:23], v[208:215], v[92:95], v189, v188 op_sel_hi:[0,0,0]
	v_mfma_scale_f32_16x16x128_f8f6f4 v[84:87], v[24:31], v[208:215], v[84:87], v189, v188 op_sel_hi:[0,0,0]
	v_mfma_scale_f32_16x16x128_f8f6f4 v[76:79], v[16:23], v[216:223], v[76:79], v189, v188 op_sel_hi:[0,0,0]
	v_mfma_scale_f32_16x16x128_f8f6f4 v[68:71], v[24:31], v[216:223], v[68:71], v189, v188 op_sel_hi:[0,0,0]
	v_mfma_scale_f32_16x16x128_f8f6f4 v[60:63], v[16:23], v[224:231], v[60:63], v189, v188 op_sel_hi:[0,0,0]
	v_mfma_scale_f32_16x16x128_f8f6f4 v[52:55], v[24:31], v[224:231], v[52:55], v189, v188 op_sel_hi:[0,0,0]
	v_mfma_scale_f32_16x16x128_f8f6f4 v[44:47], v[16:23], v[232:239], v[44:47], v189, v188 op_sel_hi:[0,0,0]
	v_mfma_scale_f32_16x16x128_f8f6f4 v[36:39], v[24:31], v[232:239], v[36:39], v189, v188 op_sel_hi:[0,0,0]
	s_setprio 0
	s_setprio 1
	v_mfma_scale_f32_16x16x128_f8f6f4 v[88:91], v[0:7], v[208:215], v[88:91], v189, v188 op_sel_hi:[0,0,0]
	v_mfma_scale_f32_16x16x128_f8f6f4 v[80:83], v[8:15], v[208:215], v[80:83], v189, v188 op_sel_hi:[0,0,0]
	v_mfma_scale_f32_16x16x128_f8f6f4 v[72:75], v[0:7], v[216:223], v[72:75], v189, v188 op_sel_hi:[0,0,0]
	v_mfma_scale_f32_16x16x128_f8f6f4 v[64:67], v[8:15], v[216:223], v[64:67], v189, v188 op_sel_hi:[0,0,0]
	v_mfma_scale_f32_16x16x128_f8f6f4 v[56:59], v[0:7], v[224:231], v[56:59], v189, v188 op_sel_hi:[0,0,0]
	v_mfma_scale_f32_16x16x128_f8f6f4 v[48:51], v[8:15], v[224:231], v[48:51], v189, v188 op_sel_hi:[0,0,0]
	v_mfma_scale_f32_16x16x128_f8f6f4 v[40:43], v[0:7], v[232:239], v[40:43], v189, v188 op_sel_hi:[0,0,0]
	v_mfma_scale_f32_16x16x128_f8f6f4 v[32:35], v[8:15], v[232:239], v[32:35], v189, v188 op_sel_hi:[0,0,0]
	s_setprio 0
	s_barrier
	s_add_i32 s63, 0, 0x18000
	s_add_i32 s64, 0, 0x1c000
	v_add_u32_e32 v0, s63, v191
	v_add_u32_e32 v1, s63, v192
	v_add_u32_e32 v4, s64, v191
	v_add_u32_e32 v12, s64, v192
	ds_read_b128 v[16:19], v0
	ds_read_b128 v[24:27], v0 offset:2048
	ds_read_b128 v[20:23], v1
	ds_read_b128 v[28:31], v1 offset:2048
	ds_read_b128 v[0:3], v4
	ds_read_b128 v[8:11], v4 offset:2048
	ds_read_b128 v[4:7], v12
	ds_read_b128 v[12:15], v12 offset:2048
	s_add_u32 s18, s18, 0x80000
	s_addc_u32 s19, s19, 0
	s_mov_b32 m0, s56
	v_lshl_add_u64 v[170:171], s[18:19], 0, v[166:167]
	ds_read_b128 v[208:211], v194 offset:32768
	ds_read_b128 v[216:219], v194 offset:34816
	ds_read_b128 v[212:215], v195 offset:32768
	ds_read_b128 v[220:223], v195 offset:34816
	ds_read_b128 v[224:227], v194 offset:36864
	ds_read_b128 v[232:235], v194 offset:38912
	ds_read_b128 v[228:231], v195 offset:36864
	ds_read_b128 v[236:239], v195 offset:38912
	global_load_lds_dwordx4 v[170:171], off
	v_lshl_add_u64 v[170:171], s[18:19], 0, v[164:165]
	s_mov_b32 m0, s57
	s_nop 0
	global_load_lds_dwordx4 v[170:171], off
	s_waitcnt vmcnt(8)
	s_waitcnt lgkmcnt(0)
	s_barrier
	s_setprio 1
	s_waitcnt lgkmcnt(0)
	v_mfma_scale_f32_16x16x128_f8f6f4 v[158:161], v[16:23], v[208:215], v[158:161], v189, v188 op_sel_hi:[0,0,0]
	v_mfma_scale_f32_16x16x128_f8f6f4 v[150:153], v[24:31], v[208:215], v[150:153], v189, v188 op_sel_hi:[0,0,0]
	v_mfma_scale_f32_16x16x128_f8f6f4 v[142:145], v[16:23], v[216:223], v[142:145], v189, v188 op_sel_hi:[0,0,0]
	v_mfma_scale_f32_16x16x128_f8f6f4 v[134:137], v[24:31], v[216:223], v[134:137], v189, v188 op_sel_hi:[0,0,0]
	v_mfma_scale_f32_16x16x128_f8f6f4 v[126:129], v[16:23], v[224:231], v[126:129], v189, v188 op_sel_hi:[0,0,0]
	v_mfma_scale_f32_16x16x128_f8f6f4 v[118:121], v[24:31], v[224:231], v[118:121], v189, v188 op_sel_hi:[0,0,0]
	v_mfma_scale_f32_16x16x128_f8f6f4 v[110:113], v[16:23], v[232:239], v[110:113], v189, v188 op_sel_hi:[0,0,0]
	v_mfma_scale_f32_16x16x128_f8f6f4 v[102:105], v[24:31], v[232:239], v[102:105], v189, v188 op_sel_hi:[0,0,0]
	s_setprio 0
	s_setprio 1
	v_mfma_scale_f32_16x16x128_f8f6f4 v[154:157], v[0:7], v[208:215], v[154:157], v189, v188 op_sel_hi:[0,0,0]
	v_mfma_scale_f32_16x16x128_f8f6f4 v[146:149], v[8:15], v[208:215], v[146:149], v189, v188 op_sel_hi:[0,0,0]
	v_mfma_scale_f32_16x16x128_f8f6f4 v[138:141], v[0:7], v[216:223], v[138:141], v189, v188 op_sel_hi:[0,0,0]
	v_mfma_scale_f32_16x16x128_f8f6f4 v[130:133], v[8:15], v[216:223], v[130:133], v189, v188 op_sel_hi:[0,0,0]
	v_mfma_scale_f32_16x16x128_f8f6f4 v[122:125], v[0:7], v[224:231], v[122:125], v189, v188 op_sel_hi:[0,0,0]
	v_mfma_scale_f32_16x16x128_f8f6f4 v[114:117], v[8:15], v[224:231], v[114:117], v189, v188 op_sel_hi:[0,0,0]
	v_mfma_scale_f32_16x16x128_f8f6f4 v[106:109], v[0:7], v[232:239], v[106:109], v189, v188 op_sel_hi:[0,0,0]
	v_mfma_scale_f32_16x16x128_f8f6f4 v[98:101], v[8:15], v[232:239], v[98:101], v189, v188 op_sel_hi:[0,0,0]
	s_setprio 0
	s_barrier
	s_add_i32 s18, s63, s59
	v_lshl_add_u64 v[170:171], v[180:181], 0, s[96:97]
	s_mov_b32 m0, s18
	ds_read_b128 v[208:211], v194 offset:49152
	ds_read_b128 v[216:219], v194 offset:51200
	ds_read_b128 v[212:215], v195 offset:49152
	ds_read_b128 v[220:223], v195 offset:51200
	ds_read_b128 v[224:227], v194 offset:53248
	ds_read_b128 v[232:235], v194 offset:55296
	ds_read_b128 v[228:231], v195 offset:53248
	ds_read_b128 v[236:239], v195 offset:55296
	global_load_lds_dwordx4 v[170:171], off
	s_add_i32 m0, s18, 0x2000
	s_add_u32 s16, s16, 0x80080
	v_lshl_add_u64 v[170:171], v[182:183], 0, s[96:97]
	s_addc_u32 s17, s17, 0
	s_add_i32 s18, s64, s59
	global_load_lds_dwordx4 v[170:171], off
	v_lshl_add_u64 v[170:171], s[16:17], 0, v[96:97]
	s_mov_b32 m0, s18
	s_nop 0
	global_load_lds_dwordx4 v[170:171], off
	v_lshl_add_u64 v[170:171], s[16:17], 0, v[162:163]
	s_add_i32 m0, s18, 0x2000
	s_nop 0
	global_load_lds_dwordx4 v[170:171], off
	v_lshl_add_u64 v[170:171], v[184:185], 0, s[96:97]
	s_mov_b32 m0, s48
	s_nop 0
	global_load_lds_dwordx4 v[170:171], off
	v_lshl_add_u64 v[170:171], v[186:187], 0, s[96:97]
	s_mov_b32 m0, s49
	s_nop 0
	global_load_lds_dwordx4 v[170:171], off
	s_waitcnt vmcnt(8)
	s_waitcnt lgkmcnt(0)
	s_barrier
	s_setprio 1
	s_waitcnt lgkmcnt(0)
	v_mfma_scale_f32_16x16x128_f8f6f4 v[92:95], v[16:23], v[208:215], v[92:95], v189, v188 op_sel_hi:[0,0,0]
	v_mfma_scale_f32_16x16x128_f8f6f4 v[84:87], v[24:31], v[208:215], v[84:87], v189, v188 op_sel_hi:[0,0,0]
	v_mfma_scale_f32_16x16x128_f8f6f4 v[76:79], v[16:23], v[216:223], v[76:79], v189, v188 op_sel_hi:[0,0,0]
	s_add_i32 s61, s61, 2
	s_add_u32 s14, s14, 0x100
	v_mfma_scale_f32_16x16x128_f8f6f4 v[68:71], v[24:31], v[216:223], v[68:71], v189, v188 op_sel_hi:[0,0,0]
	s_addc_u32 s15, s15, 0
	s_add_u32 s1, s1, 0x100
	v_mfma_scale_f32_16x16x128_f8f6f4 v[60:63], v[16:23], v[224:231], v[60:63], v189, v188 op_sel_hi:[0,0,0]
	s_addc_u32 s7, s7, 0
	s_add_u32 s16, s14, 0xfff80080
	v_mfma_scale_f32_16x16x128_f8f6f4 v[52:55], v[24:31], v[224:231], v[52:55], v189, v188 op_sel_hi:[0,0,0]
	s_addc_u32 s17, s15, -1
	s_add_i32 s63, 0, 0x10000
	v_mfma_scale_f32_16x16x128_f8f6f4 v[44:47], v[16:23], v[232:239], v[44:47], v189, v188 op_sel_hi:[0,0,0]
	s_cmp_eq_u32 s61, 28
	s_cselect_b32 s19, s9, s17
	v_mfma_scale_f32_16x16x128_f8f6f4 v[36:39], v[24:31], v[232:239], v[36:39], v189, v188 op_sel_hi:[0,0,0]
	s_cselect_b32 s18, s8, s16
	s_cselect_b32 s17, s11, s7
	s_setprio 0
	s_setprio 1
	v_mfma_scale_f32_16x16x128_f8f6f4 v[88:91], v[0:7], v[208:215], v[88:91], v189, v188 op_sel_hi:[0,0,0]
	s_cselect_b32 s16, s10, s1
	s_add_i32 s64, 0, 0x14000
	v_mfma_scale_f32_16x16x128_f8f6f4 v[80:83], v[8:15], v[208:215], v[80:83], v189, v188 op_sel_hi:[0,0,0]
	s_cmp_gt_u32 s61, 29
	v_mfma_scale_f32_16x16x128_f8f6f4 v[72:75], v[0:7], v[216:223], v[72:75], v189, v188 op_sel_hi:[0,0,0]
	v_mfma_scale_f32_16x16x128_f8f6f4 v[64:67], v[8:15], v[216:223], v[64:67], v189, v188 op_sel_hi:[0,0,0]
	v_mfma_scale_f32_16x16x128_f8f6f4 v[56:59], v[0:7], v[224:231], v[56:59], v189, v188 op_sel_hi:[0,0,0]
	v_mfma_scale_f32_16x16x128_f8f6f4 v[48:51], v[8:15], v[224:231], v[48:51], v189, v188 op_sel_hi:[0,0,0]
	v_mfma_scale_f32_16x16x128_f8f6f4 v[40:43], v[0:7], v[232:239], v[40:43], v189, v188 op_sel_hi:[0,0,0]
	v_mfma_scale_f32_16x16x128_f8f6f4 v[32:35], v[8:15], v[232:239], v[32:35], v189, v188 op_sel_hi:[0,0,0]
	s_setprio 0
	s_barrier
	s_cbranch_scc0 .Lrot_dgu
	s_and_b64 vcc, exec, s[36:37]
	s_cbranch_vccz .LBB0_786
	s_barrier

.Lrot_mdn:
	v_add_u32_e32 v0, s57, v191
	v_add_u32_e32 v1, s57, v192
	v_add_u32_e32 v4, s59, v191
	v_add_u32_e32 v12, s59, v192
	ds_read_b128 v[16:19], v0
	ds_read_b128 v[24:27], v0 offset:2048
	ds_read_b128 v[20:23], v1
	ds_read_b128 v[28:31], v1 offset:2048
	ds_read_b128 v[0:3], v4
	ds_read_b128 v[8:11], v4 offset:2048
	ds_read_b128 v[4:7], v12
	ds_read_b128 v[12:15], v12 offset:2048
	v_lshl_add_u64 v[226:227], s[22:23], 0, v[168:169]
	s_add_i32 m0, s69, 0xc000
	ds_read_b128 v[170:173], v201
	ds_read_b128 v[180:183], v201 offset:2048
	ds_read_b128 v[174:177], v208
	ds_read_b128 v[184:187], v208 offset:2048
	ds_read_b128 v[210:213], v201 offset:4096
	ds_read_b128 v[218:221], v201 offset:6144
	ds_read_b128 v[214:217], v208 offset:4096
	ds_read_b128 v[222:225], v208 offset:6144
	global_load_lds_dwordx4 v[226:227], off
	v_lshl_add_u64 v[226:227], s[22:23], 0, v[178:179]
	s_add_i32 m0, s69, 0xe000
	s_nop 0
	global_load_lds_dwordx4 v[226:227], off
	s_waitcnt vmcnt(8)
	s_waitcnt lgkmcnt(0)
	s_barrier
	s_setprio 1
	s_waitcnt lgkmcnt(0)
	v_mfma_scale_f32_16x16x128_f8f6f4 v[158:161], v[16:23], v[170:177], v[158:161], v189, v188 op_sel_hi:[0,0,0]
	v_mfma_scale_f32_16x16x128_f8f6f4 v[154:157], v[24:31], v[170:177], v[154:157], v189, v188 op_sel_hi:[0,0,0]
	v_mfma_scale_f32_16x16x128_f8f6f4 v[142:145], v[16:23], v[180:187], v[142:145], v189, v188 op_sel_hi:[0,0,0]
	v_mfma_scale_f32_16x16x128_f8f6f4 v[138:141], v[24:31], v[180:187], v[138:141], v189, v188 op_sel_hi:[0,0,0]
	v_mfma_scale_f32_16x16x128_f8f6f4 v[126:129], v[16:23], v[210:217], v[126:129], v189, v188 op_sel_hi:[0,0,0]
	v_mfma_scale_f32_16x16x128_f8f6f4 v[122:125], v[24:31], v[210:217], v[122:125], v189, v188 op_sel_hi:[0,0,0]
	v_mfma_scale_f32_16x16x128_f8f6f4 v[110:113], v[16:23], v[218:225], v[110:113], v189, v188 op_sel_hi:[0,0,0]
	v_mfma_scale_f32_16x16x128_f8f6f4 v[106:109], v[24:31], v[218:225], v[106:109], v189, v188 op_sel_hi:[0,0,0]
	s_setprio 0
	s_setprio 1
	v_mfma_scale_f32_16x16x128_f8f6f4 v[150:153], v[0:7], v[170:177], v[150:153], v189, v188 op_sel_hi:[0,0,0]
	v_mfma_scale_f32_16x16x128_f8f6f4 v[146:149], v[8:15], v[170:177], v[146:149], v189, v188 op_sel_hi:[0,0,0]
	v_mfma_scale_f32_16x16x128_f8f6f4 v[134:137], v[0:7], v[180:187], v[134:137], v189, v188 op_sel_hi:[0,0,0]
	v_mfma_scale_f32_16x16x128_f8f6f4 v[130:133], v[8:15], v[180:187], v[130:133], v189, v188 op_sel_hi:[0,0,0]
	v_mfma_scale_f32_16x16x128_f8f6f4 v[118:121], v[0:7], v[210:217], v[118:121], v189, v188 op_sel_hi:[0,0,0]
	v_mfma_scale_f32_16x16x128_f8f6f4 v[114:117], v[8:15], v[210:217], v[114:117], v189, v188 op_sel_hi:[0,0,0]
	v_mfma_scale_f32_16x16x128_f8f6f4 v[102:105], v[0:7], v[218:225], v[102:105], v189, v188 op_sel_hi:[0,0,0]
	v_mfma_scale_f32_16x16x128_f8f6f4 v[98:101], v[8:15], v[218:225], v[98:101], v189, v188 op_sel_hi:[0,0,0]
	s_setprio 0
	s_barrier
	s_add_i32 s8, s57, s48
	v_lshl_add_u64 v[180:181], s[24:25], 0, v[96:97]
	s_mov_b32 m0, s8
	ds_read_b128 v[170:173], v201 offset:16384
	ds_read_b128 v[210:213], v201 offset:18432
	ds_read_b128 v[174:177], v208 offset:16384
	ds_read_b128 v[214:217], v208 offset:18432
	ds_read_b128 v[218:221], v201 offset:20480
	ds_read_b128 v[226:229], v201 offset:22528
	ds_read_b128 v[222:225], v208 offset:20480
	ds_read_b128 v[230:233], v208 offset:22528
	global_load_lds_dwordx4 v[180:181], off
	s_add_i32 m0, s8, 0x2000
	s_add_u32 s8, s24, 0x60000
	v_lshl_add_u64 v[182:183], s[24:25], 0, v[162:163]
	s_addc_u32 s9, s25, 0
	s_add_i32 s57, s59, s48
	global_load_lds_dwordx4 v[182:183], off
	v_lshl_add_u64 v[184:185], s[8:9], 0, v[96:97]
	s_mov_b32 m0, s57
	v_lshl_add_u64 v[186:187], s[28:29], 0, v[164:165]
	global_load_lds_dwordx4 v[184:185], off
	v_lshl_add_u64 v[184:185], s[8:9], 0, v[162:163]
	s_add_i32 m0, s57, 0x2000
	s_nop 0
	global_load_lds_dwordx4 v[184:185], off
	v_lshl_add_u64 v[184:185], s[28:29], 0, v[166:167]
	s_mov_b32 m0, s69
	s_nop 0
	global_load_lds_dwordx4 v[184:185], off
	s_mov_b32 m0, s70
	s_nop 0
	global_load_lds_dwordx4 v[186:187], off
	s_waitcnt vmcnt(8)
	s_waitcnt lgkmcnt(0)
	s_barrier
	s_setprio 1
	s_waitcnt lgkmcnt(0)
	v_mfma_scale_f32_16x16x128_f8f6f4 v[92:95], v[16:23], v[170:177], v[92:95], v189, v188 op_sel_hi:[0,0,0]
	v_mfma_scale_f32_16x16x128_f8f6f4 v[88:91], v[24:31], v[170:177], v[88:91], v189, v188 op_sel_hi:[0,0,0]
	v_mfma_scale_f32_16x16x128_f8f6f4 v[76:79], v[16:23], v[210:217], v[76:79], v189, v188 op_sel_hi:[0,0,0]
	v_mfma_scale_f32_16x16x128_f8f6f4 v[72:75], v[24:31], v[210:217], v[72:75], v189, v188 op_sel_hi:[0,0,0]
	v_mfma_scale_f32_16x16x128_f8f6f4 v[60:63], v[16:23], v[218:225], v[60:63], v189, v188 op_sel_hi:[0,0,0]
	v_mfma_scale_f32_16x16x128_f8f6f4 v[56:59], v[24:31], v[218:225], v[56:59], v189, v188 op_sel_hi:[0,0,0]
	v_mfma_scale_f32_16x16x128_f8f6f4 v[44:47], v[16:23], v[226:233], v[44:47], v189, v188 op_sel_hi:[0,0,0]
	v_mfma_scale_f32_16x16x128_f8f6f4 v[40:43], v[24:31], v[226:233], v[40:43], v189, v188 op_sel_hi:[0,0,0]
	s_setprio 0
	s_setprio 1
	v_mfma_scale_f32_16x16x128_f8f6f4 v[84:87], v[0:7], v[170:177], v[84:87], v189, v188 op_sel_hi:[0,0,0]
	v_mfma_scale_f32_16x16x128_f8f6f4 v[80:83], v[8:15], v[170:177], v[80:83], v189, v188 op_sel_hi:[0,0,0]
	v_mfma_scale_f32_16x16x128_f8f6f4 v[68:71], v[0:7], v[210:217], v[68:71], v189, v188 op_sel_hi:[0,0,0]
	v_mfma_scale_f32_16x16x128_f8f6f4 v[64:67], v[8:15], v[210:217], v[64:67], v189, v188 op_sel_hi:[0,0,0]
	v_mfma_scale_f32_16x16x128_f8f6f4 v[52:55], v[0:7], v[218:225], v[52:55], v189, v188 op_sel_hi:[0,0,0]
	v_mfma_scale_f32_16x16x128_f8f6f4 v[48:51], v[8:15], v[218:225], v[48:51], v189, v188 op_sel_hi:[0,0,0]
	v_mfma_scale_f32_16x16x128_f8f6f4 v[36:39], v[0:7], v[226:233], v[36:39], v189, v188 op_sel_hi:[0,0,0]
	v_mfma_scale_f32_16x16x128_f8f6f4 v[32:35], v[8:15], v[226:233], v[32:35], v189, v188 op_sel_hi:[0,0,0]
	s_setprio 0
	s_barrier
	s_add_i32 s57, 0, 0x18000
	s_add_i32 s59, 0, 0x1c000
	v_add_u32_e32 v0, s57, v191
	v_add_u32_e32 v1, s57, v192
	v_add_u32_e32 v4, s59, v191
	v_add_u32_e32 v12, s59, v192
	ds_read_b128 v[16:19], v0
	ds_read_b128 v[24:27], v0 offset:2048
	ds_read_b128 v[20:23], v1
	ds_read_b128 v[28:31], v1 offset:2048
	ds_read_b128 v[0:3], v4
	ds_read_b128 v[8:11], v4 offset:2048
	ds_read_b128 v[4:7], v12
	ds_read_b128 v[12:15], v12 offset:2048
	s_add_u32 s8, s28, 0x60000
	s_addc_u32 s9, s29, 0
	s_mov_b32 m0, s72
	v_lshl_add_u64 v[234:235], s[8:9], 0, v[166:167]
	ds_read_b128 v[170:173], v201 offset:32768
	ds_read_b128 v[210:213], v201 offset:34816
	ds_read_b128 v[174:177], v208 offset:32768
	ds_read_b128 v[214:217], v208 offset:34816
	ds_read_b128 v[218:221], v201 offset:36864
	ds_read_b128 v[226:229], v201 offset:38912
	ds_read_b128 v[222:225], v208 offset:36864
	ds_read_b128 v[230:233], v208 offset:38912
	global_load_lds_dwordx4 v[234:235], off
	v_lshl_add_u64 v[234:235], s[8:9], 0, v[164:165]
	s_mov_b32 m0, s73
	s_nop 0
	global_load_lds_dwordx4 v[234:235], off
	s_waitcnt vmcnt(8)
	s_waitcnt lgkmcnt(0)
	s_barrier
	s_setprio 1
	s_waitcnt lgkmcnt(0)
	v_mfma_scale_f32_16x16x128_f8f6f4 v[158:161], v[16:23], v[170:177], v[158:161], v189, v188 op_sel_hi:[0,0,0]
	v_mfma_scale_f32_16x16x128_f8f6f4 v[154:157], v[24:31], v[170:177], v[154:157], v189, v188 op_sel_hi:[0,0,0]
	v_mfma_scale_f32_16x16x128_f8f6f4 v[142:145], v[16:23], v[210:217], v[142:145], v189, v188 op_sel_hi:[0,0,0]
	v_mfma_scale_f32_16x16x128_f8f6f4 v[138:141], v[24:31], v[210:217], v[138:141], v189, v188 op_sel_hi:[0,0,0]
	v_mfma_scale_f32_16x16x128_f8f6f4 v[126:129], v[16:23], v[218:225], v[126:129], v189, v188 op_sel_hi:[0,0,0]
	v_mfma_scale_f32_16x16x128_f8f6f4 v[122:125], v[24:31], v[218:225], v[122:125], v189, v188 op_sel_hi:[0,0,0]
	v_mfma_scale_f32_16x16x128_f8f6f4 v[110:113], v[16:23], v[226:233], v[110:113], v189, v188 op_sel_hi:[0,0,0]
	v_mfma_scale_f32_16x16x128_f8f6f4 v[106:109], v[24:31], v[226:233], v[106:109], v189, v188 op_sel_hi:[0,0,0]
	s_setprio 0
	s_setprio 1
	v_mfma_scale_f32_16x16x128_f8f6f4 v[150:153], v[0:7], v[170:177], v[150:153], v189, v188 op_sel_hi:[0,0,0]
	v_mfma_scale_f32_16x16x128_f8f6f4 v[146:149], v[8:15], v[170:177], v[146:149], v189, v188 op_sel_hi:[0,0,0]
	v_mfma_scale_f32_16x16x128_f8f6f4 v[134:137], v[0:7], v[210:217], v[134:137], v189, v188 op_sel_hi:[0,0,0]
	v_mfma_scale_f32_16x16x128_f8f6f4 v[130:133], v[8:15], v[210:217], v[130:133], v189, v188 op_sel_hi:[0,0,0]
	v_mfma_scale_f32_16x16x128_f8f6f4 v[118:121], v[0:7], v[218:225], v[118:121], v189, v188 op_sel_hi:[0,0,0]
	v_mfma_scale_f32_16x16x128_f8f6f4 v[114:117], v[8:15], v[218:225], v[114:117], v189, v188 op_sel_hi:[0,0,0]
	v_mfma_scale_f32_16x16x128_f8f6f4 v[102:105], v[0:7], v[226:233], v[102:105], v189, v188 op_sel_hi:[0,0,0]
	v_mfma_scale_f32_16x16x128_f8f6f4 v[98:101], v[8:15], v[226:233], v[98:101], v189, v188 op_sel_hi:[0,0,0]
	s_setprio 0
	s_barrier
	s_add_i32 s8, s57, s48
	v_lshl_add_u64 v[180:181], v[180:181], 0, s[96:97]
	s_mov_b32 m0, s8
	ds_read_b128 v[170:173], v201 offset:49152
	ds_read_b128 v[210:213], v201 offset:51200
	ds_read_b128 v[174:177], v208 offset:49152
	ds_read_b128 v[214:217], v208 offset:51200
	ds_read_b128 v[218:221], v201 offset:53248
	ds_read_b128 v[226:229], v201 offset:55296
	ds_read_b128 v[222:225], v208 offset:53248
	ds_read_b128 v[230:233], v208 offset:55296
	global_load_lds_dwordx4 v[180:181], off
	s_add_i32 m0, s8, 0x2000
	s_add_u32 s8, s24, 0x60080
	v_lshl_add_u64 v[180:181], v[182:183], 0, s[96:97]
	s_addc_u32 s9, s25, 0
	s_add_i32 s24, s59, s48
	global_load_lds_dwordx4 v[180:181], off
	v_lshl_add_u64 v[180:181], s[8:9], 0, v[96:97]
	s_mov_b32 m0, s24
	s_nop 0
	global_load_lds_dwordx4 v[180:181], off
	v_lshl_add_u64 v[180:181], s[8:9], 0, v[162:163]
	s_add_i32 m0, s24, 0x2000
	s_nop 0
	global_load_lds_dwordx4 v[180:181], off
	v_lshl_add_u64 v[180:181], v[184:185], 0, s[96:97]
	s_mov_b32 m0, s61
	s_nop 0
	global_load_lds_dwordx4 v[180:181], off
	v_lshl_add_u64 v[180:181], v[186:187], 0, s[96:97]
	s_mov_b32 m0, s77
	s_nop 0
	global_load_lds_dwordx4 v[180:181], off
	s_waitcnt vmcnt(8)
	s_waitcnt lgkmcnt(0)
	s_barrier
	s_setprio 1
	s_waitcnt lgkmcnt(0)
	v_mfma_scale_f32_16x16x128_f8f6f4 v[92:95], v[16:23], v[170:177], v[92:95], v189, v188 op_sel_hi:[0,0,0]
	v_mfma_scale_f32_16x16x128_f8f6f4 v[88:91], v[24:31], v[170:177], v[88:91], v189, v188 op_sel_hi:[0,0,0]
	v_mfma_scale_f32_16x16x128_f8f6f4 v[76:79], v[16:23], v[210:217], v[76:79], v189, v188 op_sel_hi:[0,0,0]
	s_add_i32 s56, s56, 2
	s_add_u32 s22, s22, 0x100
	v_mfma_scale_f32_16x16x128_f8f6f4 v[72:75], v[24:31], v[210:217], v[72:75], v189, v188 op_sel_hi:[0,0,0]
	s_addc_u32 s23, s23, 0
	s_add_u32 vcc_lo, vcc_lo, 0x100
	v_mfma_scale_f32_16x16x128_f8f6f4 v[60:63], v[16:23], v[218:225], v[60:63], v189, v188 op_sel_hi:[0,0,0]
	s_addc_u32 vcc_hi, vcc_hi, 0
	s_add_u32 s8, s22, 0xfffa0080
	v_mfma_scale_f32_16x16x128_f8f6f4 v[56:59], v[24:31], v[218:225], v[56:59], v189, v188 op_sel_hi:[0,0,0]
	s_addc_u32 s9, s23, -1
	s_add_i32 s57, 0, 0x10000
	v_mfma_scale_f32_16x16x128_f8f6f4 v[44:47], v[16:23], v[226:233], v[44:47], v189, v188 op_sel_hi:[0,0,0]
	s_cmp_eq_u32 s56, 20
	s_cselect_b32 s29, s17, s9
	v_mfma_scale_f32_16x16x128_f8f6f4 v[40:43], v[24:31], v[226:233], v[40:43], v189, v188 op_sel_hi:[0,0,0]
	s_cselect_b32 s28, s16, s8
	s_cselect_b32 s25, s19, vcc_hi
	s_setprio 0
	s_setprio 1
	v_mfma_scale_f32_16x16x128_f8f6f4 v[84:87], v[0:7], v[170:177], v[84:87], v189, v188 op_sel_hi:[0,0,0]
	s_cselect_b32 s24, s18, vcc_lo
	s_add_i32 s59, 0, 0x14000
	v_mfma_scale_f32_16x16x128_f8f6f4 v[80:83], v[8:15], v[170:177], v[80:83], v189, v188 op_sel_hi:[0,0,0]
	s_cmp_gt_u32 s56, 21
	v_mfma_scale_f32_16x16x128_f8f6f4 v[68:71], v[0:7], v[210:217], v[68:71], v189, v188 op_sel_hi:[0,0,0]
	v_mfma_scale_f32_16x16x128_f8f6f4 v[64:67], v[8:15], v[210:217], v[64:67], v189, v188 op_sel_hi:[0,0,0]
	v_mfma_scale_f32_16x16x128_f8f6f4 v[52:55], v[0:7], v[218:225], v[52:55], v189, v188 op_sel_hi:[0,0,0]
	v_mfma_scale_f32_16x16x128_f8f6f4 v[48:51], v[8:15], v[218:225], v[48:51], v189, v188 op_sel_hi:[0,0,0]
	v_mfma_scale_f32_16x16x128_f8f6f4 v[36:39], v[0:7], v[226:233], v[36:39], v189, v188 op_sel_hi:[0,0,0]
	v_mfma_scale_f32_16x16x128_f8f6f4 v[32:35], v[8:15], v[226:233], v[32:35], v189, v188 op_sel_hi:[0,0,0]
	s_setprio 0
	s_barrier
	s_cbranch_scc0 .Lrot_mdn
	s_and_b64 vcc, exec, s[6:7]
	s_cbranch_vccz .LBB0_860
	s_barrier

.Lrot_ddn:
	v_add_u32_e32 v0, s63, v191
	v_add_u32_e32 v1, s63, v192
	v_add_u32_e32 v4, s64, v191
	v_add_u32_e32 v12, s64, v192
	ds_read_b128 v[16:19], v0
	ds_read_b128 v[24:27], v0 offset:2048
	ds_read_b128 v[20:23], v1
	ds_read_b128 v[28:31], v1 offset:2048
	ds_read_b128 v[0:3], v4
	ds_read_b128 v[8:11], v4 offset:2048
	ds_read_b128 v[4:7], v12
	ds_read_b128 v[12:15], v12 offset:2048
	v_lshl_add_u64 v[196:197], s[12:13], 0, v[168:169]
	s_add_i32 m0, s20, 0xc000
	ds_read_b128 v[170:173], v194
	ds_read_b128 v[180:183], v194 offset:2048
	ds_read_b128 v[174:177], v195
	ds_read_b128 v[184:187], v195 offset:2048
	ds_read_b128 v[208:211], v194 offset:4096
	ds_read_b128 v[216:219], v194 offset:6144
	ds_read_b128 v[212:215], v195 offset:4096
	ds_read_b128 v[220:223], v195 offset:6144
	global_load_lds_dwordx4 v[196:197], off
	v_lshl_add_u64 v[196:197], s[12:13], 0, v[178:179]
	s_add_i32 m0, s20, 0xe000
	s_nop 0
	global_load_lds_dwordx4 v[196:197], off
	s_waitcnt vmcnt(8)
	s_waitcnt lgkmcnt(0)
	s_barrier
	s_setprio 1
	s_waitcnt lgkmcnt(0)
	v_mfma_scale_f32_16x16x128_f8f6f4 v[158:161], v[16:23], v[170:177], v[158:161], v189, v188 op_sel_hi:[0,0,0]
	v_mfma_scale_f32_16x16x128_f8f6f4 v[154:157], v[24:31], v[170:177], v[154:157], v189, v188 op_sel_hi:[0,0,0]
	v_mfma_scale_f32_16x16x128_f8f6f4 v[150:153], v[16:23], v[180:187], v[150:153], v189, v188 op_sel_hi:[0,0,0]
	v_mfma_scale_f32_16x16x128_f8f6f4 v[142:145], v[24:31], v[180:187], v[142:145], v189, v188 op_sel_hi:[0,0,0]
	v_mfma_scale_f32_16x16x128_f8f6f4 v[134:137], v[16:23], v[208:215], v[134:137], v189, v188 op_sel_hi:[0,0,0]
	v_mfma_scale_f32_16x16x128_f8f6f4 v[126:129], v[24:31], v[208:215], v[126:129], v189, v188 op_sel_hi:[0,0,0]
	v_mfma_scale_f32_16x16x128_f8f6f4 v[118:121], v[16:23], v[216:223], v[118:121], v189, v188 op_sel_hi:[0,0,0]
	v_mfma_scale_f32_16x16x128_f8f6f4 v[110:113], v[24:31], v[216:223], v[110:113], v189, v188 op_sel_hi:[0,0,0]
	s_setprio 0
	s_setprio 1
	v_mfma_scale_f32_16x16x128_f8f6f4 v[146:149], v[0:7], v[170:177], v[146:149], v189, v188 op_sel_hi:[0,0,0]
	v_mfma_scale_f32_16x16x128_f8f6f4 v[138:141], v[8:15], v[170:177], v[138:141], v189, v188 op_sel_hi:[0,0,0]
	v_mfma_scale_f32_16x16x128_f8f6f4 v[130:133], v[0:7], v[180:187], v[130:133], v189, v188 op_sel_hi:[0,0,0]
	v_mfma_scale_f32_16x16x128_f8f6f4 v[122:125], v[8:15], v[180:187], v[122:125], v189, v188 op_sel_hi:[0,0,0]
	v_mfma_scale_f32_16x16x128_f8f6f4 v[114:117], v[0:7], v[208:215], v[114:117], v189, v188 op_sel_hi:[0,0,0]
	v_mfma_scale_f32_16x16x128_f8f6f4 v[106:109], v[8:15], v[208:215], v[106:109], v189, v188 op_sel_hi:[0,0,0]
	v_mfma_scale_f32_16x16x128_f8f6f4 v[102:105], v[0:7], v[216:223], v[102:105], v189, v188 op_sel_hi:[0,0,0]
	v_mfma_scale_f32_16x16x128_f8f6f4 v[98:101], v[8:15], v[216:223], v[98:101], v189, v188 op_sel_hi:[0,0,0]
	s_setprio 0
	s_barrier
	s_add_i32 s63, s63, s48
	v_lshl_add_u64 v[180:181], s[14:15], 0, v[96:97]
	s_mov_b32 m0, s63
	ds_read_b128 v[170:173], v194 offset:16384
	ds_read_b128 v[208:211], v194 offset:18432
	ds_read_b128 v[174:177], v195 offset:16384
	ds_read_b128 v[212:215], v195 offset:18432
	ds_read_b128 v[216:219], v194 offset:20480
	ds_read_b128 v[224:227], v194 offset:22528
	ds_read_b128 v[220:223], v195 offset:20480
	ds_read_b128 v[228:231], v195 offset:22528
	global_load_lds_dwordx4 v[180:181], off
	s_add_i32 m0, s63, 0x2000
	s_add_u32 s66, s14, 0xc0000
	v_lshl_add_u64 v[182:183], s[14:15], 0, v[162:163]
	s_addc_u32 s67, s15, 0
	s_add_i32 s63, s64, s48
	global_load_lds_dwordx4 v[182:183], off
	v_lshl_add_u64 v[184:185], s[66:67], 0, v[96:97]
	s_mov_b32 m0, s63
	v_lshl_add_u64 v[186:187], s[16:17], 0, v[164:165]
	global_load_lds_dwordx4 v[184:185], off
	v_lshl_add_u64 v[184:185], s[66:67], 0, v[162:163]
	s_add_i32 m0, s63, 0x2000
	s_nop 0
	global_load_lds_dwordx4 v[184:185], off
	v_lshl_add_u64 v[184:185], s[16:17], 0, v[166:167]
	s_mov_b32 m0, s20
	s_nop 0
	global_load_lds_dwordx4 v[184:185], off
	s_mov_b32 m0, s21
	s_nop 0
	global_load_lds_dwordx4 v[186:187], off
	s_waitcnt vmcnt(8)
	s_waitcnt lgkmcnt(0)
	s_barrier
	s_setprio 1
	s_waitcnt lgkmcnt(0)
	v_mfma_scale_f32_16x16x128_f8f6f4 v[92:95], v[16:23], v[170:177], v[92:95], v189, v188 op_sel_hi:[0,0,0]
	v_mfma_scale_f32_16x16x128_f8f6f4 v[88:91], v[24:31], v[170:177], v[88:91], v189, v188 op_sel_hi:[0,0,0]
	v_mfma_scale_f32_16x16x128_f8f6f4 v[84:87], v[16:23], v[208:215], v[84:87], v189, v188 op_sel_hi:[0,0,0]
	v_mfma_scale_f32_16x16x128_f8f6f4 v[76:79], v[24:31], v[208:215], v[76:79], v189, v188 op_sel_hi:[0,0,0]
	v_mfma_scale_f32_16x16x128_f8f6f4 v[68:71], v[16:23], v[216:223], v[68:71], v189, v188 op_sel_hi:[0,0,0]
	v_mfma_scale_f32_16x16x128_f8f6f4 v[60:63], v[24:31], v[216:223], v[60:63], v189, v188 op_sel_hi:[0,0,0]
	v_mfma_scale_f32_16x16x128_f8f6f4 v[52:55], v[16:23], v[224:231], v[52:55], v189, v188 op_sel_hi:[0,0,0]
	v_mfma_scale_f32_16x16x128_f8f6f4 v[44:47], v[24:31], v[224:231], v[44:47], v189, v188 op_sel_hi:[0,0,0]
	s_setprio 0
	s_setprio 1
	v_mfma_scale_f32_16x16x128_f8f6f4 v[80:83], v[0:7], v[170:177], v[80:83], v189, v188 op_sel_hi:[0,0,0]
	v_mfma_scale_f32_16x16x128_f8f6f4 v[72:75], v[8:15], v[170:177], v[72:75], v189, v188 op_sel_hi:[0,0,0]
	v_mfma_scale_f32_16x16x128_f8f6f4 v[64:67], v[0:7], v[208:215], v[64:67], v189, v188 op_sel_hi:[0,0,0]
	v_mfma_scale_f32_16x16x128_f8f6f4 v[56:59], v[8:15], v[208:215], v[56:59], v189, v188 op_sel_hi:[0,0,0]
	v_mfma_scale_f32_16x16x128_f8f6f4 v[48:51], v[0:7], v[216:223], v[48:51], v189, v188 op_sel_hi:[0,0,0]
	v_mfma_scale_f32_16x16x128_f8f6f4 v[40:43], v[8:15], v[216:223], v[40:43], v189, v188 op_sel_hi:[0,0,0]
	v_mfma_scale_f32_16x16x128_f8f6f4 v[36:39], v[0:7], v[224:231], v[36:39], v189, v188 op_sel_hi:[0,0,0]
	v_mfma_scale_f32_16x16x128_f8f6f4 v[32:35], v[8:15], v[224:231], v[32:35], v189, v188 op_sel_hi:[0,0,0]
	s_setprio 0
	s_barrier
	s_add_i32 s63, 0, 0x18000
	s_add_i32 s64, 0, 0x1c000
	v_add_u32_e32 v0, s63, v191
	v_add_u32_e32 v1, s63, v192
	v_add_u32_e32 v4, s64, v191
	v_add_u32_e32 v12, s64, v192
	ds_read_b128 v[16:19], v0
	ds_read_b128 v[24:27], v0 offset:2048
	ds_read_b128 v[20:23], v1
	ds_read_b128 v[28:31], v1 offset:2048
	ds_read_b128 v[0:3], v4
	ds_read_b128 v[8:11], v4 offset:2048
	ds_read_b128 v[4:7], v12
	ds_read_b128 v[12:15], v12 offset:2048
	s_add_u32 s16, s16, 0xc0000
	s_addc_u32 s17, s17, 0
	s_mov_b32 m0, s22
	v_lshl_add_u64 v[196:197], s[16:17], 0, v[166:167]
	ds_read_b128 v[170:173], v194 offset:32768
	ds_read_b128 v[208:211], v194 offset:34816
	ds_read_b128 v[174:177], v195 offset:32768
	ds_read_b128 v[212:215], v195 offset:34816
	ds_read_b128 v[216:219], v194 offset:36864
	ds_read_b128 v[224:227], v194 offset:38912
	ds_read_b128 v[220:223], v195 offset:36864
	ds_read_b128 v[228:231], v195 offset:38912
	global_load_lds_dwordx4 v[196:197], off
	v_lshl_add_u64 v[196:197], s[16:17], 0, v[164:165]
	s_mov_b32 m0, s23
	s_nop 0
	global_load_lds_dwordx4 v[196:197], off
	s_waitcnt vmcnt(8)
	s_waitcnt lgkmcnt(0)
	s_barrier
	s_setprio 1
	s_waitcnt lgkmcnt(0)
	v_mfma_scale_f32_16x16x128_f8f6f4 v[158:161], v[16:23], v[170:177], v[158:161], v189, v188 op_sel_hi:[0,0,0]
	v_mfma_scale_f32_16x16x128_f8f6f4 v[154:157], v[24:31], v[170:177], v[154:157], v189, v188 op_sel_hi:[0,0,0]
	v_mfma_scale_f32_16x16x128_f8f6f4 v[150:153], v[16:23], v[208:215], v[150:153], v189, v188 op_sel_hi:[0,0,0]
	v_mfma_scale_f32_16x16x128_f8f6f4 v[142:145], v[24:31], v[208:215], v[142:145], v189, v188 op_sel_hi:[0,0,0]
	v_mfma_scale_f32_16x16x128_f8f6f4 v[134:137], v[16:23], v[216:223], v[134:137], v189, v188 op_sel_hi:[0,0,0]
	v_mfma_scale_f32_16x16x128_f8f6f4 v[126:129], v[24:31], v[216:223], v[126:129], v189, v188 op_sel_hi:[0,0,0]
	v_mfma_scale_f32_16x16x128_f8f6f4 v[118:121], v[16:23], v[224:231], v[118:121], v189, v188 op_sel_hi:[0,0,0]
	v_mfma_scale_f32_16x16x128_f8f6f4 v[110:113], v[24:31], v[224:231], v[110:113], v189, v188 op_sel_hi:[0,0,0]
	s_setprio 0
	s_setprio 1
	v_mfma_scale_f32_16x16x128_f8f6f4 v[146:149], v[0:7], v[170:177], v[146:149], v189, v188 op_sel_hi:[0,0,0]
	v_mfma_scale_f32_16x16x128_f8f6f4 v[138:141], v[8:15], v[170:177], v[138:141], v189, v188 op_sel_hi:[0,0,0]
	v_mfma_scale_f32_16x16x128_f8f6f4 v[130:133], v[0:7], v[208:215], v[130:133], v189, v188 op_sel_hi:[0,0,0]
	v_mfma_scale_f32_16x16x128_f8f6f4 v[122:125], v[8:15], v[208:215], v[122:125], v189, v188 op_sel_hi:[0,0,0]
	v_mfma_scale_f32_16x16x128_f8f6f4 v[114:117], v[0:7], v[216:223], v[114:117], v189, v188 op_sel_hi:[0,0,0]
	v_mfma_scale_f32_16x16x128_f8f6f4 v[106:109], v[8:15], v[216:223], v[106:109], v189, v188 op_sel_hi:[0,0,0]
	v_mfma_scale_f32_16x16x128_f8f6f4 v[102:105], v[0:7], v[224:231], v[102:105], v189, v188 op_sel_hi:[0,0,0]
	v_mfma_scale_f32_16x16x128_f8f6f4 v[98:101], v[8:15], v[224:231], v[98:101], v189, v188 op_sel_hi:[0,0,0]
	s_setprio 0
	s_barrier
	s_add_i32 s16, s63, s48
	v_lshl_add_u64 v[180:181], v[180:181], 0, s[96:97]
	s_mov_b32 m0, s16
	ds_read_b128 v[170:173], v194 offset:49152
	ds_read_b128 v[208:211], v194 offset:51200
	ds_read_b128 v[174:177], v195 offset:49152
	ds_read_b128 v[212:215], v195 offset:51200
	ds_read_b128 v[216:219], v194 offset:53248
	ds_read_b128 v[224:227], v194 offset:55296
	ds_read_b128 v[220:223], v195 offset:53248
	ds_read_b128 v[228:231], v195 offset:55296
	global_load_lds_dwordx4 v[180:181], off
	s_add_i32 m0, s16, 0x2000
	s_add_u32 s14, s14, 0xc0080
	v_lshl_add_u64 v[180:181], v[182:183], 0, s[96:97]
	s_addc_u32 s15, s15, 0
	s_add_i32 s16, s64, s48
	global_load_lds_dwordx4 v[180:181], off
	v_lshl_add_u64 v[180:181], s[14:15], 0, v[96:97]
	s_mov_b32 m0, s16
	s_nop 0
	global_load_lds_dwordx4 v[180:181], off
	v_lshl_add_u64 v[180:181], s[14:15], 0, v[162:163]
	s_add_i32 m0, s16, 0x2000
	s_nop 0
	global_load_lds_dwordx4 v[180:181], off
	v_lshl_add_u64 v[180:181], v[184:185], 0, s[96:97]
	s_mov_b32 m0, s24
	s_nop 0
	global_load_lds_dwordx4 v[180:181], off
	v_lshl_add_u64 v[180:181], v[186:187], 0, s[96:97]
	s_mov_b32 m0, s25
	s_nop 0
	global_load_lds_dwordx4 v[180:181], off
	s_waitcnt vmcnt(8)
	s_waitcnt lgkmcnt(0)
	s_barrier
	s_setprio 1
	s_waitcnt lgkmcnt(0)
	v_mfma_scale_f32_16x16x128_f8f6f4 v[92:95], v[16:23], v[170:177], v[92:95], v189, v188 op_sel_hi:[0,0,0]
	v_mfma_scale_f32_16x16x128_f8f6f4 v[88:91], v[24:31], v[170:177], v[88:91], v189, v188 op_sel_hi:[0,0,0]
	v_mfma_scale_f32_16x16x128_f8f6f4 v[84:87], v[16:23], v[208:215], v[84:87], v189, v188 op_sel_hi:[0,0,0]
	s_add_i32 s62, s62, 2
	s_add_u32 s12, s12, 0x100
	v_mfma_scale_f32_16x16x128_f8f6f4 v[76:79], v[24:31], v[208:215], v[76:79], v189, v188 op_sel_hi:[0,0,0]
	s_addc_u32 s13, s13, 0
	s_add_u32 s57, s57, 0x100
	v_mfma_scale_f32_16x16x128_f8f6f4 v[68:71], v[16:23], v[216:223], v[68:71], v189, v188 op_sel_hi:[0,0,0]
	s_addc_u32 s59, s59, 0
	s_add_u32 s14, s12, 0xfff40080
	v_mfma_scale_f32_16x16x128_f8f6f4 v[60:63], v[24:31], v[216:223], v[60:63], v189, v188 op_sel_hi:[0,0,0]
	s_addc_u32 s15, s13, -1
	s_add_i32 s63, 0, 0x10000
	v_mfma_scale_f32_16x16x128_f8f6f4 v[52:55], v[16:23], v[224:231], v[52:55], v189, v188 op_sel_hi:[0,0,0]
	s_cmp_eq_u32 s62, 44
	s_cselect_b32 s17, s9, s15
	v_mfma_scale_f32_16x16x128_f8f6f4 v[44:47], v[24:31], v[224:231], v[44:47], v189, v188 op_sel_hi:[0,0,0]
	s_cselect_b32 s16, s8, s14
	s_cselect_b32 s15, s11, s59
	s_setprio 0
	s_setprio 1
	v_mfma_scale_f32_16x16x128_f8f6f4 v[80:83], v[0:7], v[170:177], v[80:83], v189, v188 op_sel_hi:[0,0,0]
	s_cselect_b32 s14, s10, s57
	s_add_i32 s64, 0, 0x14000
	v_mfma_scale_f32_16x16x128_f8f6f4 v[72:75], v[8:15], v[170:177], v[72:75], v189, v188 op_sel_hi:[0,0,0]
	s_cmp_gt_u32 s62, 45
	v_mfma_scale_f32_16x16x128_f8f6f4 v[64:67], v[0:7], v[208:215], v[64:67], v189, v188 op_sel_hi:[0,0,0]
	v_mfma_scale_f32_16x16x128_f8f6f4 v[56:59], v[8:15], v[208:215], v[56:59], v189, v188 op_sel_hi:[0,0,0]
	v_mfma_scale_f32_16x16x128_f8f6f4 v[48:51], v[0:7], v[216:223], v[48:51], v189, v188 op_sel_hi:[0,0,0]
	v_mfma_scale_f32_16x16x128_f8f6f4 v[40:43], v[8:15], v[216:223], v[40:43], v189, v188 op_sel_hi:[0,0,0]
	v_mfma_scale_f32_16x16x128_f8f6f4 v[36:39], v[0:7], v[224:231], v[36:39], v189, v188 op_sel_hi:[0,0,0]
	v_mfma_scale_f32_16x16x128_f8f6f4 v[32:35], v[8:15], v[224:231], v[32:35], v189, v188 op_sel_hi:[0,0,0]
	s_setprio 0
	s_barrier
	s_cbranch_scc0 .Lrot_ddn
	s_and_b64 vcc, exec, s[6:7]
	s_cbranch_vccz .LBB0_882
	s_barrier
